# baseline (speedup 1.0000x reference)
.LBB1_42:
	s_cmp_lg_u32 s41, 0
	s_cbranch_scc0 .LBB1_46
	s_and_saveexec_b64 s[28:29], s[4:5]
	s_cbranch_execz .LBB1_45
	ds_read2_b32 v[34:35], v200 offset1:224
	ds_read2_b32 v[36:37], v234 offset1:224
	ds_read2_b32 v[38:39], v235 offset1:224
	ds_read2_b32 v[40:41], v236 offset1:224
	ds_read_b32 v42, v200 offset:448
	ds_read_b32 v43, v200 offset:1344
	ds_read_b32 v44, v234 offset:448
	ds_read_b32 v45, v234 offset:1344
	ds_read_b32 v46, v235 offset:448
	ds_read_b32 v47, v235 offset:1344
	ds_read_b32 v48, v236 offset:448
	ds_read_b32 v49, v236 offset:1344
	s_lshl_b32 s30, s56, 28
	s_add_i32 s30, s30, 0x90000000
	s_ashr_i32 s30, s30, 31
	s_and_b32 s30, s30, 0x1800
	s_waitcnt lgkmcnt(8)
	v_add_f32_e32 v34, 0, v34
	v_add_f32_e32 v34, v34, v35
	v_add_f32_e32 v34, v34, v36
	v_add_f32_e32 v34, v34, v37
	v_add_f32_e32 v34, v34, v38
	v_add_f32_e32 v34, v34, v39
	v_add_f32_e32 v34, v34, v40
	v_add_f32_e32 v34, v34, v41
	s_waitcnt lgkmcnt(0)
	v_add_f32_e32 v42, 0, v42
	v_add_f32_e32 v42, v42, v43
	v_add_f32_e32 v42, v42, v44
	v_add_f32_e32 v42, v42, v45
	v_add_f32_e32 v42, v42, v46
	v_add_f32_e32 v42, v42, v47
	v_add_f32_e32 v42, v42, v48
	v_add_f32_e32 v42, v42, v49
	v_add_u32_e32 v35, s30, v232
	ds_write_b32 v35, v34 offset:128
	ds_write_b32 v35, v42 offset:192

.LBB1_50:
	s_sub_i32 s28, 0x7e, s31
	s_mul_i32 s28, s28, 6
	s_ashr_i32 s29, s28, 31
	s_add_u32 s26, s26, s28
	s_addc_u32 s27, s27, s29
	s_cmp_lg_u32 s41, 0
	s_cselect_b64 vcc, s[74:75], s[74:75]
	s_and_b64 vcc, exec, vcc
	s_cbranch_vccnz .LBB1_59
	s_cmp_lg_u32 s41, 0
	s_cbranch_scc0 .LBB1_55
	s_and_saveexec_b64 s[28:29], s[4:5]
	s_cbranch_execz .LBB1_54
	ds_read2_b32 v[34:35], v190 offset1:224
	ds_read2_b32 v[36:37], v237 offset1:224
	ds_read2_b32 v[38:39], v238 offset1:224
	ds_read2_b32 v[40:41], v239 offset1:224
	ds_read_b32 v42, v190 offset:448
	ds_read_b32 v43, v190 offset:1344
	ds_read_b32 v44, v237 offset:448
	ds_read_b32 v45, v237 offset:1344
	ds_read_b32 v46, v238 offset:448
	ds_read_b32 v47, v238 offset:1344
	ds_read_b32 v48, v239 offset:448
	ds_read_b32 v49, v239 offset:1344
	s_lshl_b32 s30, s56, 28
	s_add_i32 s30, s30, 0xa0000000
	s_ashr_i32 s30, s30, 31
	s_and_b32 s30, s30, 0x1800
	s_waitcnt lgkmcnt(8)
	v_add_f32_e32 v34, 0, v34
	v_add_f32_e32 v34, v34, v35
	v_add_f32_e32 v34, v34, v36
	v_add_f32_e32 v34, v34, v37
	v_add_f32_e32 v34, v34, v38
	v_add_f32_e32 v34, v34, v39
	v_add_f32_e32 v34, v34, v40
	v_add_f32_e32 v34, v34, v41
	s_waitcnt lgkmcnt(0)
	v_add_f32_e32 v42, 0, v42
	v_add_f32_e32 v42, v42, v43
	v_add_f32_e32 v42, v42, v44
	v_add_f32_e32 v42, v42, v45
	v_add_f32_e32 v42, v42, v46
	v_add_f32_e32 v42, v42, v47
	v_add_f32_e32 v42, v42, v48
	v_add_f32_e32 v42, v42, v49
	v_add_u32_e32 v35, s30, v232
	ds_write_b32 v35, v34 offset:256
	ds_write_b32 v35, v42 offset:320

.LBB1_59:
	global_load_dwordx4 v[162:165], v[168:169], off
	s_waitcnt lgkmcnt(5)
	v_mfma_f32_32x32x16_f16 v[34:49], v[122:125], v[50:53], v[2:17]
	ds_read_b128 v[244:247], v179 offset:192
	v_cvt_pk_f16_f32 v166, v18, v19
	v_cvt_pk_f16_f32 v167, v20, v21
	s_waitcnt lgkmcnt(5)
	v_mfma_f32_32x32x16_f16 v[34:49], v[98:101], v[54:57], v[34:49]
	ds_read_b128 v[18:21], v179 offset:224
	v_exp_f16_e64 v50, v166 clamp
	v_exp_f16_e64 v51, v167 clamp
	v_exp_f16_sdwa v50, v166 clamp dst_sel:WORD_1 dst_unused:UNUSED_PRESERVE src0_sel:WORD_1
	v_exp_f16_sdwa v51, v167 clamp dst_sel:WORD_1 dst_unused:UNUSED_PRESERVE src0_sel:WORD_1
	s_nop 0
	s_waitcnt lgkmcnt(5)
	v_mfma_f32_32x32x16_f16 v[34:49], v[114:117], v[58:61], v[34:49]
	ds_read_b128 v[248:251], v179 offset:256
	v_pk_fma_f16 v51, v51, s55, v233 op_sel_hi:[1,0,0]
	v_pk_fma_f16 v50, v50, s55, v233 op_sel_hi:[1,0,0]
	v_pk_max_f16 v51, v167, v51
	v_pk_max_f16 v50, v166, v50
	s_waitcnt lgkmcnt(5)
	v_mfma_f32_32x32x16_f16 v[34:49], v[86:89], v[62:65], v[34:49]
	ds_read_b128 v[252:255], v179 offset:288
	v_cvt_pk_f16_f32 v52, v22, v23
	v_cvt_pk_f16_f32 v53, v24, v25
	s_waitcnt lgkmcnt(5)
	v_mfma_f32_32x32x16_f16 v[34:49], v[126:129], v[170:173], v[34:49]
	ds_read_b128 v[22:25], v179 offset:320
	v_exp_f16_e64 v54, v52 clamp
	v_exp_f16_e64 v55, v53 clamp
	v_exp_f16_sdwa v54, v52 clamp dst_sel:WORD_1 dst_unused:UNUSED_PRESERVE src0_sel:WORD_1
	v_exp_f16_sdwa v55, v53 clamp dst_sel:WORD_1 dst_unused:UNUSED_PRESERVE src0_sel:WORD_1
	s_nop 0
	s_waitcnt lgkmcnt(5)
	v_mfma_f32_32x32x16_f16 v[34:49], v[90:93], v[240:243], v[34:49]
	ds_read_b128 v[170:173], v179 offset:352
	v_pk_fma_f16 v55, v55, s55, v233 op_sel_hi:[1,0,0]
	v_pk_fma_f16 v54, v54, s55, v233 op_sel_hi:[1,0,0]
	v_pk_max_f16 v53, v53, v55
	v_pk_max_f16 v52, v52, v54
	s_waitcnt lgkmcnt(5)
	v_mfma_f32_32x32x16_f16 v[34:49], v[118:121], v[244:247], v[34:49]
	ds_read_b128 v[240:243], v179 offset:384
	v_cvt_pk_f16_f32 v166, v26, v27
	v_cvt_pk_f16_f32 v167, v28, v29
	v_mfma_f32_16x16x32_f16 v[62:65], v[70:73], v[50:53], 0
	s_waitcnt lgkmcnt(5)
	v_mfma_f32_32x32x16_f16 v[34:49], v[78:81], v[18:21], v[34:49]
	ds_read_b128 v[26:29], v179 offset:416
	v_exp_f16_e64 v244, v166 clamp
	v_exp_f16_e64 v245, v167 clamp
	v_exp_f16_sdwa v244, v166 clamp dst_sel:WORD_1 dst_unused:UNUSED_PRESERVE src0_sel:WORD_1
	v_exp_f16_sdwa v245, v167 clamp dst_sel:WORD_1 dst_unused:UNUSED_PRESERVE src0_sel:WORD_1
	s_nop 0
	s_waitcnt lgkmcnt(5)
	v_mfma_f32_32x32x16_f16 v[34:49], v[102:105], v[248:251], v[34:49]
	ds_read_b128 v[18:21], v179 offset:448
	v_pk_fma_f16 v245, v245, s55, v233 op_sel_hi:[1,0,0]
	s_nop 0
	v_pk_max_f16 v245, v167, v245
	v_pk_fma_f16 v167, v244, s55, v233 op_sel_hi:[1,0,0]
	s_nop 0
	v_pk_max_f16 v244, v166, v167
	s_waitcnt lgkmcnt(5)
	v_mfma_f32_32x32x16_f16 v[34:49], v[74:77], v[252:255], v[34:49]
	ds_read_b128 v[248:251], v179 offset:480
	v_cvt_pk_f16_f32 v30, v30, v31
	v_cvt_pk_f16_f32 v31, v32, v33
	s_waitcnt lgkmcnt(5)
	v_mfma_f32_32x32x16_f16 v[34:49], v[106:109], v[22:25], v[34:49]
	v_exp_f16_e64 v32, v30 clamp
	v_exp_f16_e64 v33, v31 clamp
	v_exp_f16_sdwa v32, v30 clamp dst_sel:WORD_1 dst_unused:UNUSED_PRESERVE src0_sel:WORD_1
	v_exp_f16_sdwa v33, v31 clamp dst_sel:WORD_1 dst_unused:UNUSED_PRESERVE src0_sel:WORD_1
	s_nop 0
	s_waitcnt lgkmcnt(4)
	v_mfma_f32_32x32x16_f16 v[34:49], v[82:85], v[170:173], v[34:49]
	v_pk_fma_f16 v22, v33, s55, v233 op_sel_hi:[1,0,0]
	s_nop 0
	v_pk_max_f16 v247, v31, v22
	v_pk_fma_f16 v22, v32, s55, v233 op_sel_hi:[1,0,0]
	s_nop 0
	v_pk_max_f16 v246, v30, v22
	s_waitcnt lgkmcnt(3)
	v_mfma_f32_32x32x16_f16 v[34:49], v[110:113], v[240:243], v[34:49]
	s_waitcnt vmcnt(2)
	v_pk_add_f16 v24, v154, v146
	v_pk_add_f16 v25, v155, v147
	s_nop 0
	v_pk_mul_f16 v22, v156, v148 clamp
	v_pk_mul_f16 v23, v157, v149 clamp
	v_pk_max_f16 v22, v24, v22
	v_pk_max_f16 v23, v25, v23
	ds_write_b64 v189, v[22:23] offset:33792
	v_mfma_f32_16x16x32_f16 v[62:65], v[66:69], v[244:247], v[62:65]
	s_waitcnt lgkmcnt(3)
	v_mfma_f32_32x32x16_f16 v[34:49], v[94:97], v[26:29], v[34:49]
	v_pk_add_f16 v24, v154, v138
	v_pk_add_f16 v25, v155, v139
	s_nop 0
	v_pk_mul_f16 v22, v156, v140 clamp
	v_pk_mul_f16 v23, v157, v141 clamp
	v_pk_max_f16 v22, v24, v22
	v_pk_max_f16 v23, v25, v23
	ds_write_b64 v189, v[22:23] offset:34320
	s_waitcnt lgkmcnt(3)
	v_mfma_f32_32x32x16_f16 v[34:49], v[134:137], v[18:21], v[34:49]
	v_pk_add_f16 v24, v154, v150
	v_pk_add_f16 v25, v155, v151
	s_nop 0
	v_pk_mul_f16 v22, v156, v152 clamp
	v_pk_mul_f16 v23, v157, v153 clamp
	v_pk_max_f16 v22, v24, v22
	v_pk_max_f16 v23, v25, v23
	ds_write_b64 v189, v[22:23] offset:34848
	s_waitcnt lgkmcnt(3)
	v_mfma_f32_32x32x16_f16 v[34:49], v[130:133], v[248:251], v[34:49]
	v_pk_add_f16 v20, v154, v142
	v_pk_add_f16 v21, v155, v143
	s_nop 0
	v_pk_mul_f16 v18, v156, v144 clamp
	v_pk_mul_f16 v19, v157, v145 clamp
	v_pk_max_f16 v18, v20, v18
	v_pk_max_f16 v19, v21, v19
	ds_write_b64 v189, v[18:19] offset:35376
	ds_write2_b32 v229, v62, v63 offset1:1
	s_and_saveexec_b64 s[28:29], s[0:1]
	ds_write2_b32 v229, v64, v65 offset0:2 offset1:3
	s_or_b64 exec, exec, s[28:29]
	v_lshl_add_u64 v[166:167], s[20:21], 4, v[168:169]
	global_load_dwordx4 v[154:157], v[166:167], off
	ds_read_b128 v[50:53], v179 offset:16896
	ds_read_b128 v[54:57], v179 offset:16928
	ds_read_b128 v[58:61], v179 offset:16960
	ds_read_b128 v[62:65], v179 offset:16992
	ds_read_b128 v[168:171], v179 offset:17024
	ds_read_b128 v[240:243], v179 offset:17056
	s_waitcnt lgkmcnt(5)
	v_mfma_f32_32x32x16_f16 v[18:33], v[122:125], v[50:53], v[2:17]
	ds_read_b128 v[244:247], v179 offset:17088
	v_cvt_pk_f16_f32 v172, v34, v35
	v_cvt_pk_f16_f32 v173, v36, v37
	s_waitcnt lgkmcnt(5)
	v_mfma_f32_32x32x16_f16 v[18:33], v[98:101], v[54:57], v[18:33]
	ds_read_b128 v[34:37], v179 offset:17120
	v_exp_f16_e64 v50, v172 clamp
	v_exp_f16_e64 v51, v173 clamp
	v_exp_f16_sdwa v50, v172 clamp dst_sel:WORD_1 dst_unused:UNUSED_PRESERVE src0_sel:WORD_1
	v_exp_f16_sdwa v51, v173 clamp dst_sel:WORD_1 dst_unused:UNUSED_PRESERVE src0_sel:WORD_1
	s_nop 0
	s_waitcnt lgkmcnt(5)
	v_mfma_f32_32x32x16_f16 v[18:33], v[114:117], v[58:61], v[18:33]
	ds_read_b128 v[248:251], v179 offset:17152
	v_pk_fma_f16 v51, v51, s55, v233 op_sel_hi:[1,0,0]
	v_pk_fma_f16 v50, v50, s55, v233 op_sel_hi:[1,0,0]
	v_pk_max_f16 v51, v173, v51
	v_pk_max_f16 v50, v172, v50
	s_waitcnt lgkmcnt(5)
	v_mfma_f32_32x32x16_f16 v[18:33], v[86:89], v[62:65], v[18:33]
	ds_read_b128 v[252:255], v179 offset:17184
	v_cvt_pk_f16_f32 v52, v38, v39
	v_cvt_pk_f16_f32 v53, v40, v41
	s_waitcnt lgkmcnt(5)
	v_mfma_f32_32x32x16_f16 v[18:33], v[126:129], v[168:171], v[18:33]
	ds_read_b128 v[38:41], v179 offset:17216
	v_exp_f16_e64 v54, v52 clamp
	v_exp_f16_e64 v55, v53 clamp
	v_exp_f16_sdwa v54, v52 clamp dst_sel:WORD_1 dst_unused:UNUSED_PRESERVE src0_sel:WORD_1
	v_exp_f16_sdwa v55, v53 clamp dst_sel:WORD_1 dst_unused:UNUSED_PRESERVE src0_sel:WORD_1
	s_nop 0
	s_waitcnt lgkmcnt(5)
	v_mfma_f32_32x32x16_f16 v[18:33], v[90:93], v[240:243], v[18:33]
	ds_read_b128 v[168:171], v179 offset:17248
	v_pk_fma_f16 v55, v55, s55, v233 op_sel_hi:[1,0,0]
	v_pk_fma_f16 v54, v54, s55, v233 op_sel_hi:[1,0,0]
	v_pk_max_f16 v53, v53, v55
	v_pk_max_f16 v52, v52, v54
	s_waitcnt lgkmcnt(5)
	v_mfma_f32_32x32x16_f16 v[18:33], v[118:121], v[244:247], v[18:33]
	ds_read_b128 v[240:243], v179 offset:17280
	v_cvt_pk_f16_f32 v172, v42, v43
	v_cvt_pk_f16_f32 v173, v44, v45
	v_mfma_f32_16x16x32_f16 v[62:65], v[70:73], v[50:53], 0
	s_waitcnt lgkmcnt(5)
	v_mfma_f32_32x32x16_f16 v[18:33], v[78:81], v[34:37], v[18:33]
	ds_read_b128 v[42:45], v179 offset:17312
	v_exp_f16_e64 v244, v172 clamp
	v_exp_f16_e64 v245, v173 clamp
	v_exp_f16_sdwa v244, v172 clamp dst_sel:WORD_1 dst_unused:UNUSED_PRESERVE src0_sel:WORD_1
	v_exp_f16_sdwa v245, v173 clamp dst_sel:WORD_1 dst_unused:UNUSED_PRESERVE src0_sel:WORD_1
	s_nop 0
	s_waitcnt lgkmcnt(5)
	v_mfma_f32_32x32x16_f16 v[18:33], v[102:105], v[248:251], v[18:33]
	ds_read_b128 v[34:37], v179 offset:17344
	v_pk_fma_f16 v245, v245, s55, v233 op_sel_hi:[1,0,0]
	s_nop 0
	v_pk_max_f16 v245, v173, v245
	v_pk_fma_f16 v173, v244, s55, v233 op_sel_hi:[1,0,0]
	s_nop 0
	v_pk_max_f16 v244, v172, v173
	s_waitcnt lgkmcnt(5)
	v_mfma_f32_32x32x16_f16 v[18:33], v[74:77], v[252:255], v[18:33]
	ds_read_b128 v[248:251], v179 offset:17376
	v_cvt_pk_f16_f32 v46, v46, v47
	v_cvt_pk_f16_f32 v47, v48, v49
	s_waitcnt lgkmcnt(5)
	v_mfma_f32_32x32x16_f16 v[18:33], v[106:109], v[38:41], v[18:33]
	v_exp_f16_e64 v48, v46 clamp
	v_exp_f16_e64 v49, v47 clamp
	v_exp_f16_sdwa v48, v46 clamp dst_sel:WORD_1 dst_unused:UNUSED_PRESERVE src0_sel:WORD_1
	v_exp_f16_sdwa v49, v47 clamp dst_sel:WORD_1 dst_unused:UNUSED_PRESERVE src0_sel:WORD_1
	s_nop 0
	s_waitcnt lgkmcnt(4)
	v_mfma_f32_32x32x16_f16 v[18:33], v[82:85], v[168:171], v[18:33]
	v_pk_fma_f16 v38, v49, s55, v233 op_sel_hi:[1,0,0]
	s_nop 0
	v_pk_max_f16 v247, v47, v38
	v_pk_fma_f16 v38, v48, s55, v233 op_sel_hi:[1,0,0]
	s_nop 0
	v_pk_max_f16 v246, v46, v38
	s_waitcnt lgkmcnt(3)
	v_mfma_f32_32x32x16_f16 v[18:33], v[110:113], v[240:243], v[18:33]
	s_waitcnt vmcnt(2)
	v_pk_add_f16 v40, v158, v146
	v_pk_add_f16 v41, v159, v147
	s_nop 0
	v_pk_mul_f16 v38, v160, v148 clamp
	v_pk_mul_f16 v39, v161, v149 clamp
	v_pk_max_f16 v38, v40, v38
	v_pk_max_f16 v39, v41, v39
	ds_write_b64 v189, v[38:39] offset:50688
	v_mfma_f32_16x16x32_f16 v[62:65], v[66:69], v[244:247], v[62:65]
	s_waitcnt lgkmcnt(3)
	v_mfma_f32_32x32x16_f16 v[18:33], v[94:97], v[42:45], v[18:33]
	v_pk_add_f16 v40, v158, v138
	v_pk_add_f16 v41, v159, v139
	s_nop 0
	v_pk_mul_f16 v38, v160, v140 clamp
	v_pk_mul_f16 v39, v161, v141 clamp
	v_pk_max_f16 v38, v40, v38
	v_pk_max_f16 v39, v41, v39
	ds_write_b64 v189, v[38:39] offset:51216
	s_waitcnt lgkmcnt(3)
	v_mfma_f32_32x32x16_f16 v[18:33], v[134:137], v[34:37], v[18:33]
	v_pk_add_f16 v40, v158, v150
	v_pk_add_f16 v41, v159, v151
	s_nop 0
	v_pk_mul_f16 v38, v160, v152 clamp
	v_pk_mul_f16 v39, v161, v153 clamp
	v_pk_max_f16 v38, v40, v38
	v_pk_max_f16 v39, v41, v39
	ds_write_b64 v189, v[38:39] offset:51744
	s_waitcnt lgkmcnt(3)
	v_mfma_f32_32x32x16_f16 v[18:33], v[130:133], v[248:251], v[18:33]
	v_pk_add_f16 v36, v158, v142
	v_pk_add_f16 v37, v159, v143
	s_nop 0
	v_pk_mul_f16 v34, v160, v144 clamp
	v_pk_mul_f16 v35, v161, v145 clamp
	v_pk_max_f16 v34, v36, v34
	v_pk_max_f16 v35, v37, v35
	ds_write_b64 v189, v[34:35] offset:52272
	ds_write2_b32 v206, v62, v63 offset1:1
	s_and_saveexec_b64 s[28:29], s[0:1]
	ds_write2_b32 v206, v64, v65 offset0:2 offset1:3
	s_or_b64 exec, exec, s[28:29]
	s_sub_i32 s28, 0x7d, s31
	s_mul_i32 s28, s28, 6
	s_ashr_i32 s29, s28, 31
	s_add_u32 s26, s26, s28
	s_addc_u32 s27, s27, s29
	s_and_b64 vcc, exec, s[8:9]
	s_waitcnt lgkmcnt(0)
	s_barrier
	ds_read_b128 v[50:53], v179 offset:33792
	ds_read_b128 v[54:57], v179 offset:33824
	ds_read_b128 v[58:61], v179 offset:33856
	ds_read_b128 v[62:65], v179 offset:33888
	s_cbranch_vccnz .LBB1_76
	s_cmp_lg_u32 s41, 0
	s_cbranch_scc0 .LBB1_72
	s_and_saveexec_b64 s[28:29], s[4:5]
	s_cbranch_execz .LBB1_71
	ds_read2_b32 v[34:35], v180 offset1:224
	v_add_u32_e32 v36, 0x700, v180
	ds_read2_b32 v[36:37], v36 offset1:224
	v_add_u32_e32 v38, 0xe00, v180
	ds_read2_b32 v[38:39], v38 offset1:224
	v_add_u32_e32 v40, 0x1500, v180
	ds_read2_b32 v[40:41], v40 offset1:224
	ds_read_b32 v42, v180 offset:448
	ds_read_b32 v43, v180 offset:1344
	ds_read_b32 v44, v180 offset:2240
	ds_read_b32 v45, v180 offset:3136
	ds_read_b32 v46, v180 offset:4032
	ds_read_b32 v47, v180 offset:4928
	ds_read_b32 v48, v180 offset:5824
	ds_read_b32 v49, v180 offset:6720
	s_lshl_b32 s30, s56, 28
	s_add_i32 s30, s30, 0xb0000000
	s_ashr_i32 s30, s30, 31
	s_and_b32 s30, s30, 0x1800
	s_waitcnt lgkmcnt(8)
	v_add_f32_e32 v34, 0, v34
	v_add_f32_e32 v34, v34, v35
	v_add_f32_e32 v34, v34, v36
	v_add_f32_e32 v34, v34, v37
	v_add_f32_e32 v34, v34, v38
	v_add_f32_e32 v34, v34, v39
	v_add_f32_e32 v34, v34, v40
	v_add_f32_e32 v34, v34, v41
	s_waitcnt lgkmcnt(0)
	v_add_f32_e32 v42, 0, v42
	v_add_f32_e32 v42, v42, v43
	v_add_f32_e32 v42, v42, v44
	v_add_f32_e32 v42, v42, v45
	v_add_f32_e32 v42, v42, v46
	v_add_f32_e32 v42, v42, v47
	v_add_f32_e32 v42, v42, v48
	v_add_f32_e32 v42, v42, v49
	v_add_u32_e32 v35, s30, v232
	ds_write_b32 v35, v34 offset:384
	ds_write_b32 v35, v42 offset:448

.LBB1_76:
	s_add_i32 s57, s31, 1
	s_sub_i32 s28, 0x7d, s57
	s_mul_i32 s28, s28, 6
	s_ashr_i32 s29, s28, 31
	s_add_u32 s28, s26, s28
	s_addc_u32 s29, s27, s29
	s_cmp_lg_u32 s41, 0
	s_cselect_b64 vcc, s[74:75], s[74:75]
	s_and_b64 vcc, exec, vcc
	s_cbranch_vccnz .LBB1_85
	s_cmp_lg_u32 s41, 0
	s_cbranch_scc0 .LBB1_81
	s_and_saveexec_b64 s[26:27], s[4:5]
	s_cbranch_execz .LBB1_80
	ds_read2_b32 v[34:35], v216 offset1:224
	v_add_u32_e32 v36, 0x700, v216
	ds_read2_b32 v[36:37], v36 offset1:224
	v_add_u32_e32 v38, 0xe00, v216
	ds_read2_b32 v[38:39], v38 offset1:224
	v_add_u32_e32 v40, 0x1500, v216
	ds_read2_b32 v[40:41], v40 offset1:224
	ds_read_b32 v42, v216 offset:448
	ds_read_b32 v43, v216 offset:1344
	ds_read_b32 v44, v216 offset:2240
	ds_read_b32 v45, v216 offset:3136
	ds_read_b32 v46, v216 offset:4032
	ds_read_b32 v47, v216 offset:4928
	ds_read_b32 v48, v216 offset:5824
	ds_read_b32 v49, v216 offset:6720
	s_lshl_b32 s30, s56, 28
	s_add_i32 s30, s30, -2.0
	s_ashr_i32 s30, s30, 31
	s_and_b32 s30, s30, 0x1800
	s_waitcnt lgkmcnt(8)
	v_add_f32_e32 v34, 0, v34
	v_add_f32_e32 v34, v34, v35
	v_add_f32_e32 v34, v34, v36
	v_add_f32_e32 v34, v34, v37
	v_add_f32_e32 v34, v34, v38
	v_add_f32_e32 v34, v34, v39
	v_add_f32_e32 v34, v34, v40
	v_add_f32_e32 v34, v34, v41
	s_waitcnt lgkmcnt(0)
	v_add_f32_e32 v42, 0, v42
	v_add_f32_e32 v42, v42, v43
	v_add_f32_e32 v42, v42, v44
	v_add_f32_e32 v42, v42, v45
	v_add_f32_e32 v42, v42, v46
	v_add_f32_e32 v42, v42, v47
	v_add_f32_e32 v42, v42, v48
	v_add_f32_e32 v42, v42, v49
	v_add_u32_e32 v35, s30, v232
	ds_write_b32 v35, v34 offset:512
	ds_write_b32 v35, v42 offset:576

.LBB1_93:
	v_lshl_add_u64 v[158:159], s[20:21], 4, v[166:167]
	global_load_dwordx4 v[170:173], v[158:159], off
	ds_read_b128 v[166:169], v179 offset:33920
	ds_read_b128 v[240:243], v179 offset:33952
	s_add_i32 s34, s57, 1
	s_waitcnt lgkmcnt(5)
	v_mfma_f32_32x32x16_f16 v[34:49], v[122:125], v[50:53], v[2:17]
	ds_read_b128 v[244:247], v179 offset:33984
	v_cvt_pk_f16_f32 v160, v18, v19
	v_cvt_pk_f16_f32 v161, v20, v21
	s_waitcnt lgkmcnt(5)
	v_mfma_f32_32x32x16_f16 v[34:49], v[98:101], v[54:57], v[34:49]
	ds_read_b128 v[18:21], v179 offset:34016
	v_exp_f16_e64 v50, v160 clamp
	v_exp_f16_e64 v51, v161 clamp
	v_exp_f16_sdwa v50, v160 clamp dst_sel:WORD_1 dst_unused:UNUSED_PRESERVE src0_sel:WORD_1
	v_exp_f16_sdwa v51, v161 clamp dst_sel:WORD_1 dst_unused:UNUSED_PRESERVE src0_sel:WORD_1
	s_nop 0
	s_waitcnt lgkmcnt(5)
	v_mfma_f32_32x32x16_f16 v[34:49], v[114:117], v[58:61], v[34:49]
	ds_read_b128 v[248:251], v179 offset:34048
	v_pk_fma_f16 v51, v51, s55, v233 op_sel_hi:[1,0,0]
	v_pk_fma_f16 v50, v50, s55, v233 op_sel_hi:[1,0,0]
	v_pk_max_f16 v51, v161, v51
	v_pk_max_f16 v50, v160, v50
	s_waitcnt lgkmcnt(5)
	v_mfma_f32_32x32x16_f16 v[34:49], v[86:89], v[62:65], v[34:49]
	ds_read_b128 v[252:255], v179 offset:34080
	v_cvt_pk_f16_f32 v52, v22, v23
	v_cvt_pk_f16_f32 v53, v24, v25
	s_waitcnt lgkmcnt(5)
	v_mfma_f32_32x32x16_f16 v[34:49], v[126:129], v[166:169], v[34:49]
	ds_read_b128 v[22:25], v179 offset:34112
	v_exp_f16_e64 v54, v52 clamp
	v_exp_f16_e64 v55, v53 clamp
	v_exp_f16_sdwa v54, v52 clamp dst_sel:WORD_1 dst_unused:UNUSED_PRESERVE src0_sel:WORD_1
	v_exp_f16_sdwa v55, v53 clamp dst_sel:WORD_1 dst_unused:UNUSED_PRESERVE src0_sel:WORD_1
	s_nop 0
	s_waitcnt lgkmcnt(5)
	v_mfma_f32_32x32x16_f16 v[34:49], v[90:93], v[240:243], v[34:49]
	ds_read_b128 v[166:169], v179 offset:34144
	v_pk_fma_f16 v55, v55, s55, v233 op_sel_hi:[1,0,0]
	v_pk_fma_f16 v54, v54, s55, v233 op_sel_hi:[1,0,0]
	v_pk_max_f16 v53, v53, v55
	v_pk_max_f16 v52, v52, v54
	s_waitcnt lgkmcnt(5)
	v_mfma_f32_32x32x16_f16 v[34:49], v[118:121], v[244:247], v[34:49]
	ds_read_b128 v[240:243], v179 offset:34176
	v_cvt_pk_f16_f32 v160, v26, v27
	v_cvt_pk_f16_f32 v161, v28, v29
	v_mfma_f32_16x16x32_f16 v[62:65], v[70:73], v[50:53], 0
	s_waitcnt lgkmcnt(5)
	v_mfma_f32_32x32x16_f16 v[34:49], v[78:81], v[18:21], v[34:49]
	ds_read_b128 v[26:29], v179 offset:34208
	v_exp_f16_e64 v244, v160 clamp
	v_exp_f16_e64 v245, v161 clamp
	v_exp_f16_sdwa v244, v160 clamp dst_sel:WORD_1 dst_unused:UNUSED_PRESERVE src0_sel:WORD_1
	v_exp_f16_sdwa v245, v161 clamp dst_sel:WORD_1 dst_unused:UNUSED_PRESERVE src0_sel:WORD_1
	s_nop 0
	s_waitcnt lgkmcnt(5)
	v_mfma_f32_32x32x16_f16 v[34:49], v[102:105], v[248:251], v[34:49]
	ds_read_b128 v[18:21], v179 offset:34240
	v_pk_fma_f16 v245, v245, s55, v233 op_sel_hi:[1,0,0]
	s_nop 0
	v_pk_max_f16 v245, v161, v245
	v_pk_fma_f16 v161, v244, s55, v233 op_sel_hi:[1,0,0]
	s_nop 0
	v_pk_max_f16 v244, v160, v161
	s_waitcnt lgkmcnt(5)
	v_mfma_f32_32x32x16_f16 v[34:49], v[74:77], v[252:255], v[34:49]
	ds_read_b128 v[248:251], v179 offset:34272
	v_cvt_pk_f16_f32 v30, v30, v31
	v_cvt_pk_f16_f32 v31, v32, v33
	s_waitcnt lgkmcnt(5)
	v_mfma_f32_32x32x16_f16 v[34:49], v[106:109], v[22:25], v[34:49]
	v_exp_f16_e64 v32, v30 clamp
	v_exp_f16_e64 v33, v31 clamp
	v_exp_f16_sdwa v32, v30 clamp dst_sel:WORD_1 dst_unused:UNUSED_PRESERVE src0_sel:WORD_1
	v_exp_f16_sdwa v33, v31 clamp dst_sel:WORD_1 dst_unused:UNUSED_PRESERVE src0_sel:WORD_1
	s_nop 0
	s_waitcnt lgkmcnt(4)
	v_mfma_f32_32x32x16_f16 v[34:49], v[82:85], v[166:169], v[34:49]
	v_pk_fma_f16 v22, v33, s55, v233 op_sel_hi:[1,0,0]
	s_nop 0
	v_pk_max_f16 v247, v31, v22
	v_pk_fma_f16 v22, v32, s55, v233 op_sel_hi:[1,0,0]
	s_nop 0
	v_pk_max_f16 v246, v30, v22
	s_waitcnt lgkmcnt(3)
	v_mfma_f32_32x32x16_f16 v[34:49], v[110:113], v[240:243], v[34:49]
	s_waitcnt vmcnt(2)
	v_pk_add_f16 v24, v146, v162
	v_pk_add_f16 v25, v147, v163
	s_nop 0
	v_pk_mul_f16 v22, v164, v148 clamp
	v_pk_mul_f16 v23, v165, v149 clamp
	v_pk_max_f16 v22, v24, v22
	v_pk_max_f16 v23, v25, v23
	ds_write_b64 v189, v[22:23]
	v_mfma_f32_16x16x32_f16 v[62:65], v[66:69], v[244:247], v[62:65]
	s_waitcnt lgkmcnt(3)
	v_mfma_f32_32x32x16_f16 v[34:49], v[94:97], v[26:29], v[34:49]
	v_pk_add_f16 v24, v138, v162
	v_pk_add_f16 v25, v139, v163
	s_nop 0
	v_pk_mul_f16 v22, v164, v140 clamp
	v_pk_mul_f16 v23, v165, v141 clamp
	v_pk_max_f16 v22, v24, v22
	v_pk_max_f16 v23, v25, v23
	ds_write_b64 v189, v[22:23] offset:528
	s_waitcnt lgkmcnt(3)
	v_mfma_f32_32x32x16_f16 v[34:49], v[134:137], v[18:21], v[34:49]
	v_pk_add_f16 v24, v150, v162
	v_pk_add_f16 v25, v151, v163
	s_nop 0
	v_pk_mul_f16 v22, v164, v152 clamp
	v_pk_mul_f16 v23, v165, v153 clamp
	v_pk_max_f16 v22, v24, v22
	v_pk_max_f16 v23, v25, v23
	ds_write_b64 v189, v[22:23] offset:1056
	s_waitcnt lgkmcnt(3)
	v_mfma_f32_32x32x16_f16 v[34:49], v[130:133], v[248:251], v[34:49]
	s_waitcnt vmcnt(1)
	v_pk_add_f16 v20, v142, v162
	v_pk_add_f16 v21, v143, v163
	s_nop 0
	v_pk_mul_f16 v18, v164, v144 clamp
	v_pk_mul_f16 v19, v165, v145 clamp
	v_pk_max_f16 v18, v20, v18
	v_pk_max_f16 v19, v21, v19
	ds_write_b64 v189, v[18:19] offset:1584
	ds_write2_b32 v201, v62, v63 offset1:1
	s_and_saveexec_b64 s[30:31], s[0:1]
	ds_write2_b32 v201, v64, v65 offset0:2 offset1:3
	s_or_b64 exec, exec, s[30:31]
	v_lshl_add_u64 v[158:159], s[20:21], 4, v[158:159]
	global_load_dwordx4 v[166:169], v[158:159], off
	ds_read_b128 v[50:53], v179 offset:50688
	ds_read_b128 v[54:57], v179 offset:50720
	ds_read_b128 v[58:61], v179 offset:50752
	ds_read_b128 v[62:65], v179 offset:50784
	ds_read_b128 v[160:163], v179 offset:50816
	ds_read_b128 v[240:243], v179 offset:50848
	s_waitcnt lgkmcnt(5)
	v_mfma_f32_32x32x16_f16 v[18:33], v[122:125], v[50:53], v[2:17]
	ds_read_b128 v[244:247], v179 offset:50880
	v_cvt_pk_f16_f32 v164, v34, v35
	v_cvt_pk_f16_f32 v165, v36, v37
	s_waitcnt lgkmcnt(5)
	v_mfma_f32_32x32x16_f16 v[18:33], v[98:101], v[54:57], v[18:33]
	ds_read_b128 v[34:37], v179 offset:50912
	v_exp_f16_e64 v50, v164 clamp
	v_exp_f16_e64 v51, v165 clamp
	v_exp_f16_sdwa v50, v164 clamp dst_sel:WORD_1 dst_unused:UNUSED_PRESERVE src0_sel:WORD_1
	v_exp_f16_sdwa v51, v165 clamp dst_sel:WORD_1 dst_unused:UNUSED_PRESERVE src0_sel:WORD_1
	s_nop 0
	s_waitcnt lgkmcnt(5)
	v_mfma_f32_32x32x16_f16 v[18:33], v[114:117], v[58:61], v[18:33]
	ds_read_b128 v[248:251], v179 offset:50944
	v_pk_fma_f16 v51, v51, s55, v233 op_sel_hi:[1,0,0]
	v_pk_fma_f16 v50, v50, s55, v233 op_sel_hi:[1,0,0]
	v_pk_max_f16 v51, v165, v51
	v_pk_max_f16 v50, v164, v50
	s_waitcnt lgkmcnt(5)
	v_mfma_f32_32x32x16_f16 v[18:33], v[86:89], v[62:65], v[18:33]
	ds_read_b128 v[252:255], v179 offset:50976
	v_cvt_pk_f16_f32 v52, v38, v39
	v_cvt_pk_f16_f32 v53, v40, v41
	s_waitcnt lgkmcnt(5)
	v_mfma_f32_32x32x16_f16 v[18:33], v[126:129], v[160:163], v[18:33]
	ds_read_b128 v[38:41], v179 offset:51008
	v_exp_f16_e64 v54, v52 clamp
	v_exp_f16_e64 v55, v53 clamp
	v_exp_f16_sdwa v54, v52 clamp dst_sel:WORD_1 dst_unused:UNUSED_PRESERVE src0_sel:WORD_1
	v_exp_f16_sdwa v55, v53 clamp dst_sel:WORD_1 dst_unused:UNUSED_PRESERVE src0_sel:WORD_1
	s_nop 0
	s_waitcnt lgkmcnt(5)
	v_mfma_f32_32x32x16_f16 v[18:33], v[90:93], v[240:243], v[18:33]
	ds_read_b128 v[160:163], v179 offset:51040
	v_pk_fma_f16 v55, v55, s55, v233 op_sel_hi:[1,0,0]
	v_pk_fma_f16 v54, v54, s55, v233 op_sel_hi:[1,0,0]
	v_pk_max_f16 v53, v53, v55
	v_pk_max_f16 v52, v52, v54
	s_waitcnt lgkmcnt(5)
	v_mfma_f32_32x32x16_f16 v[18:33], v[118:121], v[244:247], v[18:33]
	ds_read_b128 v[240:243], v179 offset:51072
	v_cvt_pk_f16_f32 v164, v42, v43
	v_cvt_pk_f16_f32 v165, v44, v45
	v_mfma_f32_16x16x32_f16 v[62:65], v[70:73], v[50:53], 0
	s_waitcnt lgkmcnt(5)
	v_mfma_f32_32x32x16_f16 v[18:33], v[78:81], v[34:37], v[18:33]
	ds_read_b128 v[42:45], v179 offset:51104
	v_exp_f16_e64 v244, v164 clamp
	v_exp_f16_e64 v245, v165 clamp
	v_exp_f16_sdwa v244, v164 clamp dst_sel:WORD_1 dst_unused:UNUSED_PRESERVE src0_sel:WORD_1
	v_exp_f16_sdwa v245, v165 clamp dst_sel:WORD_1 dst_unused:UNUSED_PRESERVE src0_sel:WORD_1
	s_nop 0
	s_waitcnt lgkmcnt(5)
	v_mfma_f32_32x32x16_f16 v[18:33], v[102:105], v[248:251], v[18:33]
	ds_read_b128 v[34:37], v179 offset:51136
	v_pk_fma_f16 v245, v245, s55, v233 op_sel_hi:[1,0,0]
	s_nop 0
	v_pk_max_f16 v245, v165, v245
	v_pk_fma_f16 v165, v244, s55, v233 op_sel_hi:[1,0,0]
	s_nop 0
	v_pk_max_f16 v244, v164, v165
	s_waitcnt lgkmcnt(5)
	v_mfma_f32_32x32x16_f16 v[18:33], v[74:77], v[252:255], v[18:33]
	ds_read_b128 v[248:251], v179 offset:51168
	v_cvt_pk_f16_f32 v46, v46, v47
	v_cvt_pk_f16_f32 v47, v48, v49
	s_waitcnt lgkmcnt(5)
	v_mfma_f32_32x32x16_f16 v[18:33], v[106:109], v[38:41], v[18:33]
	v_exp_f16_e64 v48, v46 clamp
	v_exp_f16_e64 v49, v47 clamp
	v_exp_f16_sdwa v48, v46 clamp dst_sel:WORD_1 dst_unused:UNUSED_PRESERVE src0_sel:WORD_1
	v_exp_f16_sdwa v49, v47 clamp dst_sel:WORD_1 dst_unused:UNUSED_PRESERVE src0_sel:WORD_1
	s_nop 0
	s_waitcnt lgkmcnt(4)
	v_mfma_f32_32x32x16_f16 v[18:33], v[82:85], v[160:163], v[18:33]
	v_pk_fma_f16 v38, v49, s55, v233 op_sel_hi:[1,0,0]
	s_nop 0
	v_pk_max_f16 v247, v47, v38
	v_pk_fma_f16 v38, v48, s55, v233 op_sel_hi:[1,0,0]
	s_nop 0
	v_pk_max_f16 v246, v46, v38
	s_waitcnt lgkmcnt(3)
	v_mfma_f32_32x32x16_f16 v[18:33], v[110:113], v[240:243], v[18:33]
	v_pk_add_f16 v40, v146, v154
	v_pk_add_f16 v41, v147, v155
	s_nop 0
	v_pk_mul_f16 v38, v156, v148 clamp
	v_pk_mul_f16 v39, v157, v149 clamp
	v_pk_max_f16 v38, v40, v38
	v_pk_max_f16 v39, v41, v39
	ds_write_b64 v189, v[38:39] offset:16896
	v_mfma_f32_16x16x32_f16 v[62:65], v[66:69], v[244:247], v[62:65]
	s_waitcnt lgkmcnt(3)
	v_mfma_f32_32x32x16_f16 v[18:33], v[94:97], v[42:45], v[18:33]
	v_pk_add_f16 v40, v138, v154
	v_pk_add_f16 v41, v139, v155
	s_nop 0
	v_pk_mul_f16 v38, v156, v140 clamp
	v_pk_mul_f16 v39, v157, v141 clamp
	v_pk_max_f16 v38, v40, v38
	v_pk_max_f16 v39, v41, v39
	ds_write_b64 v189, v[38:39] offset:17424
	s_waitcnt lgkmcnt(3)
	v_mfma_f32_32x32x16_f16 v[18:33], v[134:137], v[34:37], v[18:33]
	v_pk_add_f16 v40, v150, v154
	v_pk_add_f16 v41, v151, v155
	s_nop 0
	v_pk_mul_f16 v38, v156, v152 clamp
	v_pk_mul_f16 v39, v157, v153 clamp
	v_pk_max_f16 v38, v40, v38
	v_pk_max_f16 v39, v41, v39
	ds_write_b64 v189, v[38:39] offset:17952
	s_waitcnt lgkmcnt(3)
	v_mfma_f32_32x32x16_f16 v[18:33], v[130:133], v[248:251], v[18:33]
	v_pk_add_f16 v36, v142, v154
	v_pk_add_f16 v37, v143, v155
	s_nop 0
	v_pk_mul_f16 v34, v156, v144 clamp
	v_pk_mul_f16 v35, v157, v145 clamp
	v_pk_max_f16 v34, v36, v34
	v_pk_max_f16 v35, v37, v35
	ds_write_b64 v189, v[34:35] offset:18480
	ds_write2_b32 v211, v62, v63 offset1:1
	s_and_saveexec_b64 s[30:31], s[0:1]
	ds_write2_b32 v211, v64, v65 offset0:2 offset1:3
	s_or_b64 exec, exec, s[30:31]
	s_sub_i32 s30, 0x7d, s34
	s_mul_i32 s30, s30, 6
	s_ashr_i32 s31, s30, 31
	s_add_u32 s28, s28, s30
	s_addc_u32 s29, s29, s31
	s_and_b64 vcc, exec, s[8:9]
	s_waitcnt lgkmcnt(0)
	s_barrier
	ds_read_b128 v[50:53], v179
	ds_read_b128 v[54:57], v179 offset:32
	ds_read_b128 v[58:61], v179 offset:64
	ds_read_b128 v[62:65], v179 offset:96
	ds_read_b128 v[162:165], v179 offset:128
	ds_read_b128 v[240:243], v179 offset:160
	s_cbranch_vccnz .LBB1_110
	s_cmp_eq_u32 s41, 0
	s_cbranch_scc1 .LBB1_106
	s_and_saveexec_b64 s[30:31], s[4:5]
	s_cbranch_execz .LBB1_105
	ds_read2_b32 v[34:35], v200 offset1:224
	ds_read2_b32 v[36:37], v234 offset1:224
	ds_read2_b32 v[38:39], v235 offset1:224
	ds_read2_b32 v[40:41], v236 offset1:224
	ds_read_b32 v42, v200 offset:448
	ds_read_b32 v43, v200 offset:1344
	ds_read_b32 v44, v234 offset:448
	ds_read_b32 v45, v234 offset:1344
	ds_read_b32 v46, v235 offset:448
	ds_read_b32 v47, v235 offset:1344
	ds_read_b32 v48, v236 offset:448
	ds_read_b32 v49, v236 offset:1344
	s_lshl_b32 s35, s56, 28
	s_add_i32 s35, s35, 0xd0000000
	s_ashr_i32 s35, s35, 31
	s_and_b32 s35, s35, 0x1800
	s_waitcnt lgkmcnt(8)
	v_add_f32_e32 v34, 0, v34
	v_add_f32_e32 v34, v34, v35
	v_add_f32_e32 v34, v34, v36
	v_add_f32_e32 v34, v34, v37
	v_add_f32_e32 v34, v34, v38
	v_add_f32_e32 v34, v34, v39
	v_add_f32_e32 v34, v34, v40
	v_add_f32_e32 v34, v34, v41
	s_waitcnt lgkmcnt(0)
	v_add_f32_e32 v42, 0, v42
	v_add_f32_e32 v42, v42, v43
	v_add_f32_e32 v42, v42, v44
	v_add_f32_e32 v42, v42, v45
	v_add_f32_e32 v42, v42, v46
	v_add_f32_e32 v42, v42, v47
	v_add_f32_e32 v42, v42, v48
	v_add_f32_e32 v42, v42, v49
	v_add_u32_e32 v35, s35, v232
	ds_write_b32 v35, v34 offset:640
	ds_write_b32 v35, v42 offset:704

.LBB1_110:
	s_add_i32 s34, s34, 1
	s_sub_i32 s30, 0x7d, s34
	s_mul_i32 s30, s30, 6
	s_ashr_i32 s31, s30, 31
	s_add_u32 s28, s28, s30
	s_addc_u32 s29, s29, s31
	s_cmp_lg_u32 s41, 0
	s_cselect_b64 vcc, s[74:75], s[74:75]
	s_and_b64 vcc, exec, vcc
	s_cbranch_vccnz .LBB1_119
	s_cmp_eq_u32 s41, 0
	s_cbranch_scc1 .LBB1_115
	s_and_saveexec_b64 s[30:31], s[4:5]
	s_cbranch_execz .LBB1_114
	ds_read2_b32 v[34:35], v190 offset1:224
	ds_read2_b32 v[36:37], v237 offset1:224
	ds_read2_b32 v[38:39], v238 offset1:224
	ds_read2_b32 v[40:41], v239 offset1:224
	ds_read_b32 v42, v190 offset:448
	ds_read_b32 v43, v190 offset:1344
	ds_read_b32 v44, v237 offset:448
	ds_read_b32 v45, v237 offset:1344
	ds_read_b32 v46, v238 offset:448
	ds_read_b32 v47, v238 offset:1344
	ds_read_b32 v48, v239 offset:448
	ds_read_b32 v49, v239 offset:1344
	s_lshl_b32 s35, s56, 28
	s_add_i32 s35, s35, 0xe0000000
	s_ashr_i32 s35, s35, 31
	s_and_b32 s35, s35, 0x1800
	s_waitcnt lgkmcnt(8)
	v_add_f32_e32 v34, 0, v34
	v_add_f32_e32 v34, v34, v35
	v_add_f32_e32 v34, v34, v36
	v_add_f32_e32 v34, v34, v37
	v_add_f32_e32 v34, v34, v38
	v_add_f32_e32 v34, v34, v39
	v_add_f32_e32 v34, v34, v40
	v_add_f32_e32 v34, v34, v41
	s_waitcnt lgkmcnt(0)
	v_add_f32_e32 v42, 0, v42
	v_add_f32_e32 v42, v42, v43
	v_add_f32_e32 v42, v42, v44
	v_add_f32_e32 v42, v42, v45
	v_add_f32_e32 v42, v42, v46
	v_add_f32_e32 v42, v42, v47
	v_add_f32_e32 v42, v42, v48
	v_add_f32_e32 v42, v42, v49
	v_add_u32_e32 v35, s35, v232
	ds_write_b32 v35, v34 offset:768
	ds_write_b32 v35, v42 offset:832

.Lw2_sw_skip:
	v_lshl_add_u64 v[154:155], s[20:21], 4, v[154:155]
	global_load_dwordx4 v[162:165], v[154:155], off
	ds_read_b128 v[50:53], v179 offset:16896
	ds_read_b128 v[54:57], v179 offset:16928
	ds_read_b128 v[58:61], v179 offset:16960
	ds_read_b128 v[62:65], v179 offset:16992
	ds_read_b128 v[170:173], v179 offset:17024
	ds_read_b128 v[240:243], v179 offset:17056
	s_waitcnt lgkmcnt(5)
	v_mfma_f32_32x32x16_f16 v[18:33], v[122:125], v[50:53], v[2:17]
	ds_read_b128 v[244:247], v179 offset:17088
	v_cvt_pk_f16_f32 v156, v34, v35
	v_cvt_pk_f16_f32 v157, v36, v37
	s_waitcnt lgkmcnt(5)
	v_mfma_f32_32x32x16_f16 v[18:33], v[98:101], v[54:57], v[18:33]
	ds_read_b128 v[34:37], v179 offset:17120
	v_exp_f16_e64 v50, v156 clamp
	v_exp_f16_e64 v51, v157 clamp
	v_exp_f16_sdwa v50, v156 clamp dst_sel:WORD_1 dst_unused:UNUSED_PRESERVE src0_sel:WORD_1
	v_exp_f16_sdwa v51, v157 clamp dst_sel:WORD_1 dst_unused:UNUSED_PRESERVE src0_sel:WORD_1
	s_nop 0
	s_waitcnt lgkmcnt(5)
	v_mfma_f32_32x32x16_f16 v[18:33], v[114:117], v[58:61], v[18:33]
	ds_read_b128 v[248:251], v179 offset:17152
	v_pk_fma_f16 v51, v51, s55, v233 op_sel_hi:[1,0,0]
	v_pk_fma_f16 v50, v50, s55, v233 op_sel_hi:[1,0,0]
	v_pk_max_f16 v51, v157, v51
	v_pk_max_f16 v50, v156, v50
	s_waitcnt lgkmcnt(5)
	v_mfma_f32_32x32x16_f16 v[18:33], v[86:89], v[62:65], v[18:33]
	ds_read_b128 v[252:255], v179 offset:17184
	v_cvt_pk_f16_f32 v52, v38, v39
	v_cvt_pk_f16_f32 v53, v40, v41
	s_waitcnt lgkmcnt(5)
	v_mfma_f32_32x32x16_f16 v[18:33], v[126:129], v[170:173], v[18:33]
	ds_read_b128 v[38:41], v179 offset:17216
	v_exp_f16_e64 v54, v52 clamp
	v_exp_f16_e64 v55, v53 clamp
	v_exp_f16_sdwa v54, v52 clamp dst_sel:WORD_1 dst_unused:UNUSED_PRESERVE src0_sel:WORD_1
	v_exp_f16_sdwa v55, v53 clamp dst_sel:WORD_1 dst_unused:UNUSED_PRESERVE src0_sel:WORD_1
	s_nop 0
	s_waitcnt lgkmcnt(5)
	v_mfma_f32_32x32x16_f16 v[18:33], v[90:93], v[240:243], v[18:33]
	ds_read_b128 v[170:173], v179 offset:17248
	v_pk_fma_f16 v55, v55, s55, v233 op_sel_hi:[1,0,0]
	v_pk_fma_f16 v54, v54, s55, v233 op_sel_hi:[1,0,0]
	v_pk_max_f16 v53, v53, v55
	v_pk_max_f16 v52, v52, v54
	s_waitcnt lgkmcnt(5)
	v_mfma_f32_32x32x16_f16 v[18:33], v[118:121], v[244:247], v[18:33]
	ds_read_b128 v[240:243], v179 offset:17280
	v_cvt_pk_f16_f32 v156, v42, v43
	v_cvt_pk_f16_f32 v157, v44, v45
	v_mfma_f32_16x16x32_f16 v[62:65], v[70:73], v[50:53], 0
	s_waitcnt lgkmcnt(5)
	v_mfma_f32_32x32x16_f16 v[18:33], v[78:81], v[34:37], v[18:33]
	ds_read_b128 v[42:45], v179 offset:17312
	v_exp_f16_e64 v244, v156 clamp
	v_exp_f16_e64 v245, v157 clamp
	v_exp_f16_sdwa v244, v156 clamp dst_sel:WORD_1 dst_unused:UNUSED_PRESERVE src0_sel:WORD_1
	v_exp_f16_sdwa v245, v157 clamp dst_sel:WORD_1 dst_unused:UNUSED_PRESERVE src0_sel:WORD_1
	s_nop 0
	s_waitcnt lgkmcnt(5)
	v_mfma_f32_32x32x16_f16 v[18:33], v[102:105], v[248:251], v[18:33]
	ds_read_b128 v[34:37], v179 offset:17344
	v_pk_fma_f16 v245, v245, s55, v233 op_sel_hi:[1,0,0]
	s_nop 0
	v_pk_max_f16 v245, v157, v245
	v_pk_fma_f16 v157, v244, s55, v233 op_sel_hi:[1,0,0]
	s_nop 0
	v_pk_max_f16 v244, v156, v157
	s_waitcnt lgkmcnt(5)
	v_mfma_f32_32x32x16_f16 v[18:33], v[74:77], v[252:255], v[18:33]
	ds_read_b128 v[248:251], v179 offset:17376
	v_cvt_pk_f16_f32 v46, v46, v47
	v_cvt_pk_f16_f32 v47, v48, v49
	s_waitcnt lgkmcnt(5)
	v_mfma_f32_32x32x16_f16 v[18:33], v[106:109], v[38:41], v[18:33]
	v_exp_f16_e64 v48, v46 clamp
	v_exp_f16_e64 v49, v47 clamp
	v_exp_f16_sdwa v48, v46 clamp dst_sel:WORD_1 dst_unused:UNUSED_PRESERVE src0_sel:WORD_1
	v_exp_f16_sdwa v49, v47 clamp dst_sel:WORD_1 dst_unused:UNUSED_PRESERVE src0_sel:WORD_1
	s_nop 0
	s_waitcnt lgkmcnt(4)
	v_mfma_f32_32x32x16_f16 v[18:33], v[82:85], v[170:173], v[18:33]
	v_pk_fma_f16 v38, v49, s55, v233 op_sel_hi:[1,0,0]
	s_nop 0
	v_pk_max_f16 v247, v47, v38
	v_pk_fma_f16 v38, v48, s55, v233 op_sel_hi:[1,0,0]
	s_nop 0
	v_pk_max_f16 v246, v46, v38
	s_waitcnt lgkmcnt(3)
	v_mfma_f32_32x32x16_f16 v[18:33], v[110:113], v[240:243], v[18:33]
	s_waitcnt vmcnt(2)
	v_pk_add_f16 v40, v166, v146
	v_pk_add_f16 v41, v167, v147
	s_nop 0
	v_pk_mul_f16 v38, v168, v148 clamp
	v_pk_mul_f16 v39, v169, v149 clamp
	v_pk_max_f16 v38, v40, v38
	v_pk_max_f16 v39, v41, v39
	ds_write_b64 v189, v[38:39] offset:50688
	v_mfma_f32_16x16x32_f16 v[62:65], v[66:69], v[244:247], v[62:65]
	s_waitcnt lgkmcnt(3)
	v_mfma_f32_32x32x16_f16 v[18:33], v[94:97], v[42:45], v[18:33]
	v_pk_add_f16 v40, v166, v138
	v_pk_add_f16 v41, v167, v139
	s_nop 0
	v_pk_mul_f16 v38, v168, v140 clamp
	v_pk_mul_f16 v39, v169, v141 clamp
	v_pk_max_f16 v38, v40, v38
	v_pk_max_f16 v39, v41, v39
	ds_write_b64 v189, v[38:39] offset:51216
	s_waitcnt lgkmcnt(3)
	v_mfma_f32_32x32x16_f16 v[18:33], v[134:137], v[34:37], v[18:33]
	v_pk_add_f16 v40, v166, v150
	v_pk_add_f16 v41, v167, v151
	s_nop 0
	v_pk_mul_f16 v38, v168, v152 clamp
	v_pk_mul_f16 v39, v169, v153 clamp
	v_pk_max_f16 v38, v40, v38
	v_pk_max_f16 v39, v41, v39
	ds_write_b64 v189, v[38:39] offset:51744
	s_waitcnt lgkmcnt(3)
	v_mfma_f32_32x32x16_f16 v[18:33], v[130:133], v[248:251], v[18:33]
	v_pk_add_f16 v36, v166, v142
	v_pk_add_f16 v37, v167, v143
	s_nop 0
	v_pk_mul_f16 v34, v168, v144 clamp
	v_pk_mul_f16 v35, v169, v145 clamp
	v_pk_max_f16 v34, v36, v34
	v_pk_max_f16 v35, v37, v35
	ds_write_b64 v189, v[34:35] offset:52272
	ds_write2_b32 v206, v62, v63 offset1:1
	s_and_saveexec_b64 s[30:31], s[0:1]
	ds_write2_b32 v206, v64, v65 offset0:2 offset1:3
	s_or_b64 exec, exec, s[30:31]
	s_add_i32 s34, s34, 1
	s_sub_i32 s30, 0x7d, s34
	s_mul_i32 s30, s30, 6
	s_ashr_i32 s31, s30, 31
	s_add_u32 s28, s28, s30
	s_addc_u32 s29, s29, s31
	s_and_b64 vcc, exec, s[8:9]
	s_waitcnt lgkmcnt(0)
	s_barrier
	ds_read_b128 v[50:53], v179 offset:33792
	ds_read_b128 v[54:57], v179 offset:33824
	ds_read_b128 v[58:61], v179 offset:33856
	ds_read_b128 v[62:65], v179 offset:33888
	ds_read_b128 v[168:171], v179 offset:33920
	ds_read_b128 v[240:243], v179 offset:33952
	s_cbranch_vccnz .LBB1_136
	s_cmp_eq_u32 s41, 0
	s_cbranch_scc1 .LBB1_132
	s_and_saveexec_b64 s[30:31], s[4:5]
	s_cbranch_execz .LBB1_131
	ds_read2_b32 v[34:35], v180 offset1:224
	v_add_u32_e32 v36, 0x700, v180
	ds_read2_b32 v[36:37], v36 offset1:224
	v_add_u32_e32 v38, 0xe00, v180
	ds_read2_b32 v[38:39], v38 offset1:224
	v_add_u32_e32 v40, 0x1500, v180
	ds_read2_b32 v[40:41], v40 offset1:224
	ds_read_b32 v42, v180 offset:448
	ds_read_b32 v43, v180 offset:1344
	ds_read_b32 v44, v180 offset:2240
	ds_read_b32 v45, v180 offset:3136
	ds_read_b32 v46, v180 offset:4032
	ds_read_b32 v47, v180 offset:4928
	ds_read_b32 v48, v180 offset:5824
	ds_read_b32 v49, v180 offset:6720
	s_lshl_b32 s35, s56, 28
	s_add_i32 s35, s35, 0xf0000000
	s_ashr_i32 s35, s35, 31
	s_and_b32 s35, s35, 0x1800
	s_waitcnt lgkmcnt(8)
	v_add_f32_e32 v34, 0, v34
	v_add_f32_e32 v34, v34, v35
	v_add_f32_e32 v34, v34, v36
	v_add_f32_e32 v34, v34, v37
	v_add_f32_e32 v34, v34, v38
	v_add_f32_e32 v34, v34, v39
	v_add_f32_e32 v34, v34, v40
	v_add_f32_e32 v34, v34, v41
	s_waitcnt lgkmcnt(0)
	v_add_f32_e32 v42, 0, v42
	v_add_f32_e32 v42, v42, v43
	v_add_f32_e32 v42, v42, v44
	v_add_f32_e32 v42, v42, v45
	v_add_f32_e32 v42, v42, v46
	v_add_f32_e32 v42, v42, v47
	v_add_f32_e32 v42, v42, v48
	v_add_f32_e32 v42, v42, v49
	v_add_u32_e32 v35, s35, v232
	ds_write_b32 v35, v34 offset:896
	ds_write_b32 v35, v42 offset:960

.LBB1_136:
	s_add_i32 s34, s34, 1
	s_sub_i32 s30, 0x7d, s34
	s_mul_i32 s30, s30, 6
	s_ashr_i32 s31, s30, 31
	s_add_u32 s30, s28, s30
	s_addc_u32 s31, s29, s31
	s_and_b64 s[28:29], exec, s[26:27]
	s_cselect_b32 s29, s52, s31
	s_cselect_b32 s28, s53, s30
	s_cselect_b32 s41, s49, s41
	s_cmp_lg_u32 s41, 0
	s_cselect_b64 vcc, s[74:75], s[74:75]
	s_and_b64 vcc, exec, vcc
	s_cbranch_vccnz .LBB1_145
	s_cmp_eq_u32 s41, 0
	s_cbranch_scc1 .LBB1_141
	s_and_saveexec_b64 s[30:31], s[4:5]
	s_cbranch_execz .LBB1_140
	ds_read2_b32 v[34:35], v216 offset1:224
	v_add_u32_e32 v36, 0x700, v216
	ds_read2_b32 v[36:37], v36 offset1:224
	v_add_u32_e32 v38, 0xe00, v216
	ds_read2_b32 v[38:39], v38 offset1:224
	v_add_u32_e32 v40, 0x1500, v216
	ds_read2_b32 v[40:41], v40 offset1:224
	ds_read_b32 v42, v216 offset:448
	ds_read_b32 v43, v216 offset:1344
	ds_read_b32 v44, v216 offset:2240
	ds_read_b32 v45, v216 offset:3136
	ds_read_b32 v46, v216 offset:4032
	ds_read_b32 v47, v216 offset:4928
	ds_read_b32 v48, v216 offset:5824
	ds_read_b32 v49, v216 offset:6720
	s_bfe_i32 s35, s56, 0x10003
	s_and_b32 s35, s35, 0x1800
	s_waitcnt lgkmcnt(8)
	v_add_f32_e32 v34, 0, v34
	v_add_f32_e32 v34, v34, v35
	v_add_f32_e32 v34, v34, v36
	v_add_f32_e32 v34, v34, v37
	v_add_f32_e32 v34, v34, v38
	v_add_f32_e32 v34, v34, v39
	v_add_f32_e32 v34, v34, v40
	v_add_f32_e32 v34, v34, v41
	s_waitcnt lgkmcnt(0)
	v_add_f32_e32 v42, 0, v42
	v_add_f32_e32 v42, v42, v43
	v_add_f32_e32 v42, v42, v44
	v_add_f32_e32 v42, v42, v45
	v_add_f32_e32 v42, v42, v46
	v_add_f32_e32 v42, v42, v47
	v_add_f32_e32 v42, v42, v48
	v_add_f32_e32 v42, v42, v49
	v_add_u32_e32 v35, s35, v232
	ds_write_b32 v35, v34
	ds_write_b32 v35, v42 offset:64

.LBB1_155:
	ds_read_b128 v[50:53], v179
	ds_read_b128 v[54:57], v179 offset:32
	ds_read_b128 v[58:61], v179 offset:64
	ds_read_b128 v[62:65], v179 offset:96
	ds_read_b128 v[162:165], v179 offset:128
	ds_read_b128 v[166:169], v179 offset:160
	s_and_b64 vcc, exec, s[24:25]
	s_cbranch_vccz .LBB1_164
	s_cmp_lg_u32 s41, 0
	s_cbranch_scc0 .LBB1_160
	s_and_saveexec_b64 s[12:13], s[4:5]
	s_cbranch_execz .LBB1_159
	ds_read2_b32 v[34:35], v200 offset1:224
	v_add_u32_e32 v36, 0x700, v200
	ds_read2_b32 v[36:37], v36 offset1:224
	v_add_u32_e32 v38, 0xe00, v200
	ds_read2_b32 v[38:39], v38 offset1:224
	v_add_u32_e32 v40, 0x1500, v200
	ds_read2_b32 v[40:41], v40 offset1:224
	ds_read_b32 v42, v200 offset:448
	ds_read_b32 v43, v200 offset:1344
	ds_read_b32 v44, v200 offset:2240
	ds_read_b32 v45, v200 offset:3136
	ds_read_b32 v46, v200 offset:4032
	ds_read_b32 v47, v200 offset:4928
	ds_read_b32 v48, v200 offset:5824
	ds_read_b32 v49, v200 offset:6720
	s_waitcnt lgkmcnt(8)
	v_add_f32_e32 v34, 0, v34
	v_add_f32_e32 v34, v34, v35
	v_add_f32_e32 v34, v34, v36
	v_add_f32_e32 v34, v34, v37
	v_add_f32_e32 v34, v34, v38
	v_add_f32_e32 v34, v34, v39
	v_add_f32_e32 v34, v34, v40
	v_add_f32_e32 v34, v34, v41
	s_waitcnt lgkmcnt(0)
	v_add_f32_e32 v42, 0, v42
	v_add_f32_e32 v42, v42, v43
	v_add_f32_e32 v42, v42, v44
	v_add_f32_e32 v42, v42, v45
	v_add_f32_e32 v42, v42, v46
	v_add_f32_e32 v42, v42, v47
	v_add_f32_e32 v42, v42, v48
	v_add_f32_e32 v42, v42, v49
	v_mov_b32_e32 v35, 0x19080
	v_lshl_add_u32 v35, v177, 2, v35
	ds_write_b32 v35, v34
	ds_write_b32 v35, v42 offset:64

.LBB1_164:
	s_sub_i32 s12, 0x7d, s30
	s_mul_i32 s12, s12, 6
	s_ashr_i32 s13, s12, 31
	s_add_u32 s12, s26, s12
	s_addc_u32 s13, s27, s13
	s_cmp_lg_u32 s41, 0
	s_cselect_b64 vcc, s[74:75], s[74:75]
	s_and_b64 vcc, exec, vcc
	s_cbranch_vccnz .LBB1_173
	s_cmp_lg_u32 s41, 0
	s_cbranch_scc0 .LBB1_169
	s_and_saveexec_b64 s[20:21], s[4:5]
	s_cbranch_execz .LBB1_168
	ds_read2_b32 v[34:35], v190 offset1:224
	v_add_u32_e32 v36, 0x700, v190
	ds_read2_b32 v[36:37], v36 offset1:224
	v_add_u32_e32 v38, 0xe00, v190
	ds_read2_b32 v[38:39], v38 offset1:224
	v_add_u32_e32 v40, 0x1500, v190
	ds_read2_b32 v[40:41], v40 offset1:224
	ds_read_b32 v42, v190 offset:448
	ds_read_b32 v43, v190 offset:1344
	ds_read_b32 v44, v190 offset:2240
	ds_read_b32 v45, v190 offset:3136
	ds_read_b32 v46, v190 offset:4032
	ds_read_b32 v47, v190 offset:4928
	ds_read_b32 v48, v190 offset:5824
	ds_read_b32 v49, v190 offset:6720
	s_waitcnt lgkmcnt(8)
	v_add_f32_e32 v34, 0, v34
	v_add_f32_e32 v34, v34, v35
	v_add_f32_e32 v34, v34, v36
	v_add_f32_e32 v34, v34, v37
	v_add_f32_e32 v34, v34, v38
	v_add_f32_e32 v34, v34, v39
	v_add_f32_e32 v34, v34, v40
	v_add_f32_e32 v34, v34, v41
	s_waitcnt lgkmcnt(0)
	v_add_f32_e32 v42, 0, v42
	v_add_f32_e32 v42, v42, v43
	v_add_f32_e32 v42, v42, v44
	v_add_f32_e32 v42, v42, v45
	v_add_f32_e32 v42, v42, v46
	v_add_f32_e32 v42, v42, v47
	v_add_f32_e32 v42, v42, v48
	v_add_f32_e32 v42, v42, v49
	v_mov_b32_e32 v35, 0x19100
	v_lshl_add_u32 v35, v177, 2, v35
	ds_write_b32 v35, v34
	ds_write_b32 v35, v42 offset:64

.LBB1_173:
	s_waitcnt lgkmcnt(5)
	v_mfma_f32_32x32x16_f16 v[34:49], v[122:125], v[50:53], v[2:17]
	ds_read_b128 v[170:173], v179 offset:192
	v_cvt_pk_f16_f32 v174, v18, v19
	v_cvt_pk_f16_f32 v175, v20, v21
	s_waitcnt lgkmcnt(5)
	v_mfma_f32_32x32x16_f16 v[34:49], v[98:101], v[54:57], v[34:49]
	ds_read_b128 v[18:21], v179 offset:224
	v_exp_f16_e64 v50, v174 clamp
	v_exp_f16_e64 v51, v175 clamp
	v_exp_f16_sdwa v50, v174 clamp dst_sel:WORD_1 dst_unused:UNUSED_PRESERVE src0_sel:WORD_1
	v_exp_f16_sdwa v51, v175 clamp dst_sel:WORD_1 dst_unused:UNUSED_PRESERVE src0_sel:WORD_1
	s_nop 0
	s_waitcnt lgkmcnt(5)
	v_mfma_f32_32x32x16_f16 v[34:49], v[114:117], v[58:61], v[34:49]
	ds_read_b128 v[230:233], v179 offset:256
	s_movk_i32 s20, 0x3dc5
	v_mov_b32_e32 v199, 0xbdc5
	v_pk_fma_f16 v51, v51, s20, v199 op_sel_hi:[1,0,0]
	v_pk_fma_f16 v50, v50, s20, v199 op_sel_hi:[1,0,0]
	v_pk_max_f16 v51, v175, v51
	v_pk_max_f16 v50, v174, v50
	s_waitcnt lgkmcnt(5)
	v_mfma_f32_32x32x16_f16 v[34:49], v[86:89], v[62:65], v[34:49]
	ds_read_b128 v[234:237], v179 offset:288
	v_cvt_pk_f16_f32 v52, v22, v23
	v_cvt_pk_f16_f32 v53, v24, v25
	s_waitcnt lgkmcnt(5)
	v_mfma_f32_32x32x16_f16 v[34:49], v[126:129], v[162:165], v[34:49]
	ds_read_b128 v[22:25], v179 offset:320
	v_exp_f16_e64 v54, v52 clamp
	v_exp_f16_e64 v55, v53 clamp
	v_exp_f16_sdwa v54, v52 clamp dst_sel:WORD_1 dst_unused:UNUSED_PRESERVE src0_sel:WORD_1
	v_exp_f16_sdwa v55, v53 clamp dst_sel:WORD_1 dst_unused:UNUSED_PRESERVE src0_sel:WORD_1
	s_nop 0
	s_waitcnt lgkmcnt(5)
	v_mfma_f32_32x32x16_f16 v[34:49], v[90:93], v[166:169], v[34:49]
	ds_read_b128 v[162:165], v179 offset:352
	v_pk_fma_f16 v55, v55, s20, v199 op_sel_hi:[1,0,0]
	v_pk_fma_f16 v54, v54, s20, v199 op_sel_hi:[1,0,0]
	v_pk_max_f16 v53, v53, v55
	v_pk_max_f16 v52, v52, v54
	s_waitcnt lgkmcnt(5)
	v_mfma_f32_32x32x16_f16 v[34:49], v[118:121], v[170:173], v[34:49]
	ds_read_b128 v[166:169], v179 offset:384
	v_cvt_pk_f16_f32 v170, v26, v27
	v_cvt_pk_f16_f32 v171, v28, v29
	v_mfma_f32_16x16x32_f16 v[62:65], v[70:73], v[50:53], 0
	s_waitcnt lgkmcnt(5)
	v_mfma_f32_32x32x16_f16 v[34:49], v[78:81], v[18:21], v[34:49]
	ds_read_b128 v[26:29], v179 offset:416
	v_exp_f16_e64 v172, v170 clamp
	v_exp_f16_e64 v173, v171 clamp
	v_exp_f16_sdwa v172, v170 clamp dst_sel:WORD_1 dst_unused:UNUSED_PRESERVE src0_sel:WORD_1
	v_exp_f16_sdwa v173, v171 clamp dst_sel:WORD_1 dst_unused:UNUSED_PRESERVE src0_sel:WORD_1
	s_nop 0
	s_waitcnt lgkmcnt(5)
	v_mfma_f32_32x32x16_f16 v[34:49], v[102:105], v[230:233], v[34:49]
	ds_read_b128 v[18:21], v179 offset:448
	v_pk_fma_f16 v173, v173, s20, v199 op_sel_hi:[1,0,0]
	v_pk_fma_f16 v172, v172, s20, v199 op_sel_hi:[1,0,0]
	v_pk_max_f16 v171, v171, v173
	v_pk_max_f16 v170, v170, v172
	s_waitcnt lgkmcnt(5)
	v_mfma_f32_32x32x16_f16 v[34:49], v[74:77], v[234:237], v[34:49]
	ds_read_b128 v[230:233], v179 offset:480
	v_cvt_pk_f16_f32 v30, v30, v31
	v_cvt_pk_f16_f32 v31, v32, v33
	s_waitcnt lgkmcnt(5)
	v_mfma_f32_32x32x16_f16 v[34:49], v[106:109], v[22:25], v[34:49]
	v_exp_f16_e64 v32, v30 clamp
	v_exp_f16_e64 v33, v31 clamp
	v_exp_f16_sdwa v32, v30 clamp dst_sel:WORD_1 dst_unused:UNUSED_PRESERVE src0_sel:WORD_1
	v_exp_f16_sdwa v33, v31 clamp dst_sel:WORD_1 dst_unused:UNUSED_PRESERVE src0_sel:WORD_1
	s_nop 0
	s_waitcnt lgkmcnt(4)
	v_mfma_f32_32x32x16_f16 v[34:49], v[82:85], v[162:165], v[34:49]
	v_pk_fma_f16 v22, v33, s20, v199 op_sel_hi:[1,0,0]
	s_nop 0
	v_pk_max_f16 v173, v31, v22
	v_pk_fma_f16 v22, v32, s20, v199 op_sel_hi:[1,0,0]
	s_nop 0
	v_pk_max_f16 v172, v30, v22
	s_waitcnt lgkmcnt(3)
	v_mfma_f32_32x32x16_f16 v[34:49], v[110:113], v[166:169], v[34:49]
	s_waitcnt vmcnt(1)
	v_pk_add_f16 v24, v146, v154
	v_pk_add_f16 v25, v147, v155
	s_nop 0
	v_pk_mul_f16 v22, v156, v148 clamp
	v_pk_mul_f16 v23, v157, v149 clamp
	v_pk_max_f16 v22, v24, v22
	v_pk_max_f16 v23, v25, v23
	ds_write_b64 v189, v[22:23] offset:33792
	v_mfma_f32_16x16x32_f16 v[62:65], v[66:69], v[170:173], v[62:65]
	s_waitcnt lgkmcnt(3)
	v_mfma_f32_32x32x16_f16 v[34:49], v[94:97], v[26:29], v[34:49]
	v_pk_add_f16 v24, v138, v154
	v_pk_add_f16 v25, v139, v155
	s_nop 0
	v_pk_mul_f16 v22, v156, v140 clamp
	v_pk_mul_f16 v23, v157, v141 clamp
	v_pk_max_f16 v22, v24, v22
	v_pk_max_f16 v23, v25, v23
	ds_write_b64 v189, v[22:23] offset:34320
	s_waitcnt lgkmcnt(3)
	v_mfma_f32_32x32x16_f16 v[34:49], v[134:137], v[18:21], v[34:49]
	v_pk_add_f16 v24, v150, v154
	v_pk_add_f16 v25, v151, v155
	s_nop 0
	v_pk_mul_f16 v22, v156, v152 clamp
	v_pk_mul_f16 v23, v157, v153 clamp
	v_pk_max_f16 v22, v24, v22
	v_pk_max_f16 v23, v25, v23
	ds_write_b64 v189, v[22:23] offset:34848
	s_waitcnt lgkmcnt(3)
	v_mfma_f32_32x32x16_f16 v[34:49], v[130:133], v[230:233], v[34:49]
	v_pk_add_f16 v20, v142, v154
	v_pk_add_f16 v21, v143, v155
	s_nop 0
	v_pk_mul_f16 v18, v156, v144 clamp
	v_pk_mul_f16 v19, v157, v145 clamp
	v_pk_max_f16 v18, v20, v18
	v_pk_max_f16 v19, v21, v19
	ds_write_b64 v189, v[18:19] offset:35376
	ds_write2_b32 v229, v62, v63 offset1:1
	s_and_saveexec_b64 s[20:21], s[0:1]
	ds_write2_b32 v229, v64, v65 offset0:2 offset1:3
	s_or_b64 exec, exec, s[20:21]
	ds_read_b128 v[50:53], v179 offset:16896
	ds_read_b128 v[54:57], v179 offset:16928
	ds_read_b128 v[58:61], v179 offset:16960
	ds_read_b128 v[62:65], v179 offset:16992
	ds_read_b128 v[154:157], v179 offset:17024
	ds_read_b128 v[162:165], v179 offset:17056
	s_waitcnt lgkmcnt(5)
	v_mfma_f32_32x32x16_f16 v[18:33], v[122:125], v[50:53], v[2:17]
	ds_read_b128 v[166:169], v179 offset:17088
	v_cvt_pk_f16_f32 v174, v34, v35
	v_cvt_pk_f16_f32 v175, v36, v37
	s_waitcnt lgkmcnt(5)
	v_mfma_f32_32x32x16_f16 v[18:33], v[98:101], v[54:57], v[18:33]
	ds_read_b128 v[34:37], v179 offset:17120
	v_exp_f16_e64 v50, v174 clamp
	v_exp_f16_e64 v51, v175 clamp
	v_exp_f16_sdwa v50, v174 clamp dst_sel:WORD_1 dst_unused:UNUSED_PRESERVE src0_sel:WORD_1
	v_exp_f16_sdwa v51, v175 clamp dst_sel:WORD_1 dst_unused:UNUSED_PRESERVE src0_sel:WORD_1
	s_nop 0
	s_waitcnt lgkmcnt(5)
	v_mfma_f32_32x32x16_f16 v[18:33], v[114:117], v[58:61], v[18:33]
	ds_read_b128 v[170:173], v179 offset:17152
	s_movk_i32 s20, 0x3dc5
	v_mov_b32_e32 v199, 0xbdc5
	v_pk_fma_f16 v51, v51, s20, v199 op_sel_hi:[1,0,0]
	v_pk_fma_f16 v50, v50, s20, v199 op_sel_hi:[1,0,0]
	v_pk_max_f16 v51, v175, v51
	v_pk_max_f16 v50, v174, v50
	s_waitcnt lgkmcnt(5)
	v_mfma_f32_32x32x16_f16 v[18:33], v[86:89], v[62:65], v[18:33]
	ds_read_b128 v[228:231], v179 offset:17184
	v_cvt_pk_f16_f32 v52, v38, v39
	v_cvt_pk_f16_f32 v53, v40, v41
	s_waitcnt lgkmcnt(5)
	v_mfma_f32_32x32x16_f16 v[18:33], v[126:129], v[154:157], v[18:33]
	ds_read_b128 v[38:41], v179 offset:17216
	v_exp_f16_e64 v54, v52 clamp
	v_exp_f16_e64 v55, v53 clamp
	v_exp_f16_sdwa v54, v52 clamp dst_sel:WORD_1 dst_unused:UNUSED_PRESERVE src0_sel:WORD_1
	v_exp_f16_sdwa v55, v53 clamp dst_sel:WORD_1 dst_unused:UNUSED_PRESERVE src0_sel:WORD_1
	s_nop 0
	s_waitcnt lgkmcnt(5)
	v_mfma_f32_32x32x16_f16 v[18:33], v[90:93], v[162:165], v[18:33]
	ds_read_b128 v[154:157], v179 offset:17248
	v_pk_fma_f16 v55, v55, s20, v199 op_sel_hi:[1,0,0]
	v_pk_fma_f16 v54, v54, s20, v199 op_sel_hi:[1,0,0]
	v_pk_max_f16 v53, v53, v55
	v_pk_max_f16 v52, v52, v54
	s_waitcnt lgkmcnt(5)
	v_mfma_f32_32x32x16_f16 v[18:33], v[118:121], v[166:169], v[18:33]
	ds_read_b128 v[162:165], v179 offset:17280
	v_cvt_pk_f16_f32 v166, v42, v43
	v_cvt_pk_f16_f32 v167, v44, v45
	v_mfma_f32_16x16x32_f16 v[62:65], v[70:73], v[50:53], 0
	s_waitcnt lgkmcnt(5)
	v_mfma_f32_32x32x16_f16 v[18:33], v[78:81], v[34:37], v[18:33]
	ds_read_b128 v[42:45], v179 offset:17312
	v_exp_f16_e64 v168, v166 clamp
	v_exp_f16_e64 v169, v167 clamp
	v_exp_f16_sdwa v168, v166 clamp dst_sel:WORD_1 dst_unused:UNUSED_PRESERVE src0_sel:WORD_1
	v_exp_f16_sdwa v169, v167 clamp dst_sel:WORD_1 dst_unused:UNUSED_PRESERVE src0_sel:WORD_1
	s_nop 0
	s_waitcnt lgkmcnt(5)
	v_mfma_f32_32x32x16_f16 v[18:33], v[102:105], v[170:173], v[18:33]
	ds_read_b128 v[34:37], v179 offset:17344
	v_pk_fma_f16 v169, v169, s20, v199 op_sel_hi:[1,0,0]
	v_pk_fma_f16 v168, v168, s20, v199 op_sel_hi:[1,0,0]
	v_pk_max_f16 v167, v167, v169
	v_pk_max_f16 v166, v166, v168
	s_waitcnt lgkmcnt(5)
	v_mfma_f32_32x32x16_f16 v[18:33], v[74:77], v[228:231], v[18:33]
	ds_read_b128 v[170:173], v179 offset:17376
	v_cvt_pk_f16_f32 v46, v46, v47
	v_cvt_pk_f16_f32 v47, v48, v49
	s_waitcnt lgkmcnt(5)
	v_mfma_f32_32x32x16_f16 v[18:33], v[106:109], v[38:41], v[18:33]
	v_exp_f16_e64 v48, v46 clamp
	v_exp_f16_e64 v49, v47 clamp
	v_exp_f16_sdwa v48, v46 clamp dst_sel:WORD_1 dst_unused:UNUSED_PRESERVE src0_sel:WORD_1
	v_exp_f16_sdwa v49, v47 clamp dst_sel:WORD_1 dst_unused:UNUSED_PRESERVE src0_sel:WORD_1
	s_nop 0
	s_waitcnt lgkmcnt(4)
	v_mfma_f32_32x32x16_f16 v[18:33], v[82:85], v[154:157], v[18:33]
	v_pk_fma_f16 v38, v49, s20, v199 op_sel_hi:[1,0,0]
	s_nop 0
	v_pk_max_f16 v169, v47, v38
	v_pk_fma_f16 v38, v48, s20, v199 op_sel_hi:[1,0,0]
	s_nop 0
	v_pk_max_f16 v168, v46, v38
	s_waitcnt lgkmcnt(3)
	v_mfma_f32_32x32x16_f16 v[18:33], v[110:113], v[162:165], v[18:33]
	s_waitcnt vmcnt(0)
	v_pk_add_f16 v40, v146, v158
	v_pk_add_f16 v41, v147, v159
	s_nop 0
	v_pk_mul_f16 v38, v160, v148 clamp
	v_pk_mul_f16 v39, v161, v149 clamp
	v_pk_max_f16 v38, v40, v38
	v_pk_max_f16 v39, v41, v39
	ds_write_b64 v189, v[38:39] offset:50688
	v_mfma_f32_16x16x32_f16 v[62:65], v[66:69], v[166:169], v[62:65]
	s_waitcnt lgkmcnt(3)
	v_mfma_f32_32x32x16_f16 v[18:33], v[94:97], v[42:45], v[18:33]
	v_pk_add_f16 v40, v138, v158
	v_pk_add_f16 v41, v139, v159
	s_nop 0
	v_pk_mul_f16 v38, v160, v140 clamp
	v_pk_mul_f16 v39, v161, v141 clamp
	v_pk_max_f16 v38, v40, v38
	v_pk_max_f16 v39, v41, v39
	ds_write_b64 v189, v[38:39] offset:51216
	s_waitcnt lgkmcnt(3)
	v_mfma_f32_32x32x16_f16 v[18:33], v[134:137], v[34:37], v[18:33]
	v_pk_add_f16 v40, v150, v158
	v_pk_add_f16 v41, v151, v159
	s_nop 0
	v_pk_mul_f16 v38, v160, v152 clamp
	v_pk_mul_f16 v39, v161, v153 clamp
	v_pk_max_f16 v38, v40, v38
	v_pk_max_f16 v39, v41, v39
	ds_write_b64 v189, v[38:39] offset:51744
	s_waitcnt lgkmcnt(3)
	v_mfma_f32_32x32x16_f16 v[18:33], v[130:133], v[170:173], v[18:33]
	v_pk_add_f16 v36, v142, v158
	v_pk_add_f16 v37, v143, v159
	s_nop 0
	v_pk_mul_f16 v34, v160, v144 clamp
	v_pk_mul_f16 v35, v161, v145 clamp
	v_pk_max_f16 v34, v36, v34
	v_pk_max_f16 v35, v37, v35
	ds_write_b64 v189, v[34:35] offset:52272
	ds_write2_b32 v206, v62, v63 offset1:1
	s_and_saveexec_b64 s[20:21], s[0:1]
	ds_write2_b32 v206, v64, v65 offset0:2 offset1:3
	s_or_b64 exec, exec, s[20:21]
	s_sub_i32 s20, 0x7c, s30
	s_mul_i32 s20, s20, 6
	s_ashr_i32 s21, s20, 31
	s_add_u32 s12, s12, s20
	s_addc_u32 s13, s13, s21
	s_and_b64 vcc, exec, s[8:9]
	s_waitcnt lgkmcnt(0)
	s_barrier
	s_cbranch_vccnz .LBB1_190
	s_cmp_lg_u32 s41, 0
	s_cbranch_scc0 .LBB1_186
	s_and_saveexec_b64 s[20:21], s[4:5]
	s_cbranch_execz .LBB1_185
	ds_read2_b32 v[34:35], v180 offset1:224
	v_add_u32_e32 v36, 0x700, v180
	ds_read2_b32 v[36:37], v36 offset1:224
	v_add_u32_e32 v38, 0xe00, v180
	ds_read2_b32 v[38:39], v38 offset1:224
	v_add_u32_e32 v40, 0x1500, v180
	ds_read2_b32 v[40:41], v40 offset1:224
	ds_read_b32 v42, v180 offset:448
	ds_read_b32 v43, v180 offset:1344
	ds_read_b32 v44, v180 offset:2240
	ds_read_b32 v45, v180 offset:3136
	ds_read_b32 v46, v180 offset:4032
	ds_read_b32 v47, v180 offset:4928
	ds_read_b32 v48, v180 offset:5824
	ds_read_b32 v49, v180 offset:6720
	s_waitcnt lgkmcnt(8)
	v_add_f32_e32 v34, 0, v34
	v_add_f32_e32 v34, v34, v35
	v_add_f32_e32 v34, v34, v36
	v_add_f32_e32 v34, v34, v37
	v_add_f32_e32 v34, v34, v38
	v_add_f32_e32 v34, v34, v39
	v_add_f32_e32 v34, v34, v40
	v_add_f32_e32 v34, v34, v41
	s_waitcnt lgkmcnt(0)
	v_add_f32_e32 v42, 0, v42
	v_add_f32_e32 v42, v42, v43
	v_add_f32_e32 v42, v42, v44
	v_add_f32_e32 v42, v42, v45
	v_add_f32_e32 v42, v42, v46
	v_add_f32_e32 v42, v42, v47
	v_add_f32_e32 v42, v42, v48
	v_add_f32_e32 v42, v42, v49
	v_mov_b32_e32 v35, 0x19180
	v_lshl_add_u32 v35, v177, 2, v35
	ds_write_b32 v35, v34
	ds_write_b32 v35, v42 offset:64

.LBB1_190:
	s_sub_i32 s20, 0x7b, s30
	s_mul_i32 s20, s20, 6
	s_ashr_i32 s21, s20, 31
	s_add_u32 s12, s12, s20
	s_addc_u32 s13, s13, s21
	s_cmp_lg_u32 s41, 0
	s_cselect_b64 vcc, s[74:75], s[74:75]
	s_and_b64 vcc, exec, vcc
	s_cbranch_vccnz .LBB1_199
	s_cmp_lg_u32 s41, 0
	s_cbranch_scc0 .LBB1_195
	s_and_saveexec_b64 s[20:21], s[4:5]
	s_cbranch_execz .LBB1_194
	ds_read2_b32 v[34:35], v216 offset1:224
	v_add_u32_e32 v36, 0x700, v216
	ds_read2_b32 v[36:37], v36 offset1:224
	v_add_u32_e32 v38, 0xe00, v216
	ds_read2_b32 v[38:39], v38 offset1:224
	v_add_u32_e32 v40, 0x1500, v216
	ds_read2_b32 v[40:41], v40 offset1:224
	ds_read_b32 v42, v216 offset:448
	ds_read_b32 v43, v216 offset:1344
	ds_read_b32 v44, v216 offset:2240
	ds_read_b32 v45, v216 offset:3136
	ds_read_b32 v46, v216 offset:4032
	ds_read_b32 v47, v216 offset:4928
	ds_read_b32 v48, v216 offset:5824
	ds_read_b32 v49, v216 offset:6720
	s_waitcnt lgkmcnt(8)
	v_add_f32_e32 v34, 0, v34
	v_add_f32_e32 v34, v34, v35
	v_add_f32_e32 v34, v34, v36
	v_add_f32_e32 v34, v34, v37
	v_add_f32_e32 v34, v34, v38
	v_add_f32_e32 v34, v34, v39
	v_add_f32_e32 v34, v34, v40
	v_add_f32_e32 v34, v34, v41
	s_waitcnt lgkmcnt(0)
	v_add_f32_e32 v42, 0, v42
	v_add_f32_e32 v42, v42, v43
	v_add_f32_e32 v42, v42, v44
	v_add_f32_e32 v42, v42, v45
	v_add_f32_e32 v42, v42, v46
	v_add_f32_e32 v42, v42, v47
	v_add_f32_e32 v42, v42, v48
	v_add_f32_e32 v42, v42, v49
	v_mov_b32_e32 v35, 0x19200
	v_lshl_add_u32 v35, v177, 2, v35
	ds_write_b32 v35, v34
	ds_write_b32 v35, v42 offset:64

.LBB1_199:
	ds_read_b128 v[50:53], v179 offset:33792
	ds_read_b128 v[54:57], v179 offset:33824
	ds_read_b128 v[58:61], v179 offset:33856
	ds_read_b128 v[62:65], v179 offset:33888
	ds_read_b128 v[138:141], v179 offset:33920
	ds_read_b128 v[142:145], v179 offset:33952
	s_waitcnt lgkmcnt(5)
	v_mfma_f32_32x32x16_f16 v[34:49], v[122:125], v[50:53], v[2:17]
	ds_read_b128 v[146:149], v179 offset:33984
	v_cvt_pk_f16_f32 v154, v18, v19
	v_cvt_pk_f16_f32 v155, v20, v21
	s_waitcnt lgkmcnt(5)
	v_mfma_f32_32x32x16_f16 v[34:49], v[98:101], v[54:57], v[34:49]
	ds_read_b128 v[18:21], v179 offset:34016
	v_exp_f16_e64 v50, v154 clamp
	v_exp_f16_e64 v51, v155 clamp
	v_exp_f16_sdwa v50, v154 clamp dst_sel:WORD_1 dst_unused:UNUSED_PRESERVE src0_sel:WORD_1
	v_exp_f16_sdwa v51, v155 clamp dst_sel:WORD_1 dst_unused:UNUSED_PRESERVE src0_sel:WORD_1
	s_nop 0
	s_waitcnt lgkmcnt(5)
	v_mfma_f32_32x32x16_f16 v[34:49], v[114:117], v[58:61], v[34:49]
	ds_read_b128 v[150:153], v179 offset:34048
	s_movk_i32 s20, 0x3dc5
	v_mov_b32_e32 v158, 0xbdc5
	v_pk_fma_f16 v51, v51, s20, v158 op_sel_hi:[1,0,0]
	v_pk_fma_f16 v50, v50, s20, v158 op_sel_hi:[1,0,0]
	v_pk_max_f16 v51, v155, v51
	v_pk_max_f16 v50, v154, v50
	s_waitcnt lgkmcnt(5)
	v_mfma_f32_32x32x16_f16 v[34:49], v[86:89], v[62:65], v[34:49]
	ds_read_b128 v[154:157], v179 offset:34080
	v_cvt_pk_f16_f32 v52, v22, v23
	v_cvt_pk_f16_f32 v53, v24, v25
	s_waitcnt lgkmcnt(5)
	v_mfma_f32_32x32x16_f16 v[34:49], v[126:129], v[138:141], v[34:49]
	ds_read_b128 v[22:25], v179 offset:34112
	v_exp_f16_e64 v54, v52 clamp
	v_exp_f16_e64 v55, v53 clamp
	v_exp_f16_sdwa v54, v52 clamp dst_sel:WORD_1 dst_unused:UNUSED_PRESERVE src0_sel:WORD_1
	v_exp_f16_sdwa v55, v53 clamp dst_sel:WORD_1 dst_unused:UNUSED_PRESERVE src0_sel:WORD_1
	s_nop 0
	s_waitcnt lgkmcnt(5)
	v_mfma_f32_32x32x16_f16 v[34:49], v[90:93], v[142:145], v[34:49]
	ds_read_b128 v[138:141], v179 offset:34144
	v_pk_fma_f16 v55, v55, s20, v158 op_sel_hi:[1,0,0]
	v_pk_fma_f16 v54, v54, s20, v158 op_sel_hi:[1,0,0]
	v_pk_max_f16 v53, v53, v55
	v_pk_max_f16 v52, v52, v54
	s_waitcnt lgkmcnt(5)
	v_mfma_f32_32x32x16_f16 v[34:49], v[118:121], v[146:149], v[34:49]
	ds_read_b128 v[142:145], v179 offset:34176
	v_cvt_pk_f16_f32 v146, v26, v27
	v_cvt_pk_f16_f32 v147, v28, v29
	v_mfma_f32_16x16x32_f16 v[62:65], v[70:73], v[50:53], 0
	s_waitcnt lgkmcnt(5)
	v_mfma_f32_32x32x16_f16 v[34:49], v[78:81], v[18:21], v[34:49]
	ds_read_b128 v[26:29], v179 offset:34208
	v_exp_f16_e64 v148, v146 clamp
	v_exp_f16_e64 v149, v147 clamp
	v_exp_f16_sdwa v148, v146 clamp dst_sel:WORD_1 dst_unused:UNUSED_PRESERVE src0_sel:WORD_1
	v_exp_f16_sdwa v149, v147 clamp dst_sel:WORD_1 dst_unused:UNUSED_PRESERVE src0_sel:WORD_1
	s_nop 0
	s_waitcnt lgkmcnt(5)
	v_mfma_f32_32x32x16_f16 v[34:49], v[102:105], v[150:153], v[34:49]
	ds_read_b128 v[18:21], v179 offset:34240
	v_pk_fma_f16 v149, v149, s20, v158 op_sel_hi:[1,0,0]
	v_pk_fma_f16 v148, v148, s20, v158 op_sel_hi:[1,0,0]
	v_pk_max_f16 v147, v147, v149
	v_pk_max_f16 v146, v146, v148
	s_waitcnt lgkmcnt(5)
	v_mfma_f32_32x32x16_f16 v[34:49], v[74:77], v[154:157], v[34:49]
	ds_read_b128 v[150:153], v179 offset:34272
	v_cvt_pk_f16_f32 v30, v30, v31
	v_cvt_pk_f16_f32 v31, v32, v33
	s_waitcnt lgkmcnt(5)
	v_mfma_f32_32x32x16_f16 v[34:49], v[106:109], v[22:25], v[34:49]
	v_exp_f16_e64 v32, v30 clamp
	v_exp_f16_e64 v33, v31 clamp
	v_exp_f16_sdwa v32, v30 clamp dst_sel:WORD_1 dst_unused:UNUSED_PRESERVE src0_sel:WORD_1
	v_exp_f16_sdwa v33, v31 clamp dst_sel:WORD_1 dst_unused:UNUSED_PRESERVE src0_sel:WORD_1
	s_nop 0
	s_waitcnt lgkmcnt(4)
	v_mfma_f32_32x32x16_f16 v[34:49], v[82:85], v[138:141], v[34:49]
	v_pk_fma_f16 v22, v33, s20, v158 op_sel_hi:[1,0,0]
	s_nop 0
	v_pk_max_f16 v149, v31, v22
	v_pk_fma_f16 v22, v32, s20, v158 op_sel_hi:[1,0,0]
	s_nop 0
	v_pk_max_f16 v148, v30, v22
	s_waitcnt lgkmcnt(3)
	v_mfma_f32_32x32x16_f16 v[34:49], v[110:113], v[142:145], v[34:49]
	v_mfma_f32_16x16x32_f16 v[62:65], v[66:69], v[146:149], v[62:65]
	s_waitcnt lgkmcnt(2)
	v_mfma_f32_32x32x16_f16 v[34:49], v[94:97], v[26:29], v[34:49]
	s_waitcnt lgkmcnt(1)
	v_mfma_f32_32x32x16_f16 v[34:49], v[134:137], v[18:21], v[34:49]
	s_waitcnt lgkmcnt(0)
	v_mfma_f32_32x32x16_f16 v[34:49], v[130:133], v[150:153], v[34:49]
	s_nop 5
	ds_write2_b32 v201, v62, v63 offset1:1
	s_and_saveexec_b64 s[20:21], s[0:1]
	ds_write2_b32 v201, v64, v65 offset0:2 offset1:3
	s_or_b64 exec, exec, s[20:21]
	ds_read_b128 v[18:21], v179 offset:50688
	ds_read_b128 v[22:25], v179 offset:50720
	ds_read_b128 v[26:29], v179 offset:50752
	ds_read_b128 v[30:33], v179 offset:50784
	ds_read_b128 v[50:53], v179 offset:50816
	ds_read_b128 v[54:57], v179 offset:50848
	s_waitcnt lgkmcnt(5)
	v_mfma_f32_32x32x16_f16 v[2:17], v[122:125], v[18:21], v[2:17]
	ds_read_b128 v[58:61], v179 offset:50880
	v_cvt_pk_f16_f32 v138, v34, v35
	v_cvt_pk_f16_f32 v139, v36, v37
	s_waitcnt lgkmcnt(5)
	v_mfma_f32_32x32x16_f16 v[2:17], v[98:101], v[22:25], v[2:17]
	ds_read_b128 v[34:37], v179 offset:50912
	v_exp_f16_e64 v18, v138 clamp
	v_exp_f16_e64 v19, v139 clamp
	v_exp_f16_sdwa v18, v138 clamp dst_sel:WORD_1 dst_unused:UNUSED_PRESERVE src0_sel:WORD_1
	v_exp_f16_sdwa v19, v139 clamp dst_sel:WORD_1 dst_unused:UNUSED_PRESERVE src0_sel:WORD_1
	s_nop 0
	s_waitcnt lgkmcnt(5)
	v_mfma_f32_32x32x16_f16 v[2:17], v[114:117], v[26:29], v[2:17]
	ds_read_b128 v[62:65], v179 offset:50944
	s_movk_i32 s20, 0x3dc5
	v_mov_b32_e32 v122, 0xbdc5
	v_pk_fma_f16 v19, v19, s20, v122 op_sel_hi:[1,0,0]
	v_pk_fma_f16 v18, v18, s20, v122 op_sel_hi:[1,0,0]
	v_pk_max_f16 v19, v139, v19
	v_pk_max_f16 v18, v138, v18
	s_waitcnt lgkmcnt(5)
	v_mfma_f32_32x32x16_f16 v[2:17], v[86:89], v[30:33], v[2:17]
	ds_read_b128 v[98:101], v179 offset:50976
	v_cvt_pk_f16_f32 v20, v38, v39
	v_cvt_pk_f16_f32 v21, v40, v41
	s_waitcnt lgkmcnt(5)
	v_mfma_f32_32x32x16_f16 v[2:17], v[126:129], v[50:53], v[2:17]
	ds_read_b128 v[38:41], v179 offset:51008
	v_exp_f16_e64 v22, v20 clamp
	v_exp_f16_e64 v23, v21 clamp
	v_exp_f16_sdwa v22, v20 clamp dst_sel:WORD_1 dst_unused:UNUSED_PRESERVE src0_sel:WORD_1
	v_exp_f16_sdwa v23, v21 clamp dst_sel:WORD_1 dst_unused:UNUSED_PRESERVE src0_sel:WORD_1
	s_nop 0
	s_waitcnt lgkmcnt(5)
	v_mfma_f32_32x32x16_f16 v[2:17], v[90:93], v[54:57], v[2:17]
	ds_read_b128 v[50:53], v179 offset:51040
	v_pk_fma_f16 v23, v23, s20, v122 op_sel_hi:[1,0,0]
	v_pk_fma_f16 v22, v22, s20, v122 op_sel_hi:[1,0,0]
	v_pk_max_f16 v21, v21, v23
	v_pk_max_f16 v20, v20, v22
	s_waitcnt lgkmcnt(5)
	v_mfma_f32_32x32x16_f16 v[2:17], v[118:121], v[58:61], v[2:17]
	ds_read_b128 v[54:57], v179 offset:51072
	v_cvt_pk_f16_f32 v58, v42, v43
	v_cvt_pk_f16_f32 v59, v44, v45
	v_mfma_f32_16x16x32_f16 v[30:33], v[70:73], v[18:21], 0
	s_waitcnt lgkmcnt(5)
	v_mfma_f32_32x32x16_f16 v[2:17], v[78:81], v[34:37], v[2:17]
	ds_read_b128 v[42:45], v179 offset:51104
	v_exp_f16_e64 v60, v58 clamp
	v_exp_f16_e64 v61, v59 clamp
	v_exp_f16_sdwa v60, v58 clamp dst_sel:WORD_1 dst_unused:UNUSED_PRESERVE src0_sel:WORD_1
	v_exp_f16_sdwa v61, v59 clamp dst_sel:WORD_1 dst_unused:UNUSED_PRESERVE src0_sel:WORD_1
	s_nop 0
	s_waitcnt lgkmcnt(5)
	v_mfma_f32_32x32x16_f16 v[2:17], v[102:105], v[62:65], v[2:17]
	ds_read_b128 v[34:37], v179 offset:51136
	v_pk_fma_f16 v61, v61, s20, v122 op_sel_hi:[1,0,0]
	v_pk_fma_f16 v60, v60, s20, v122 op_sel_hi:[1,0,0]
	v_pk_max_f16 v59, v59, v61
	v_pk_max_f16 v58, v58, v60
	s_waitcnt lgkmcnt(5)
	v_mfma_f32_32x32x16_f16 v[2:17], v[74:77], v[98:101], v[2:17]
	ds_read_b128 v[62:65], v179 offset:51168
	v_cvt_pk_f16_f32 v46, v46, v47
	v_cvt_pk_f16_f32 v47, v48, v49
	s_waitcnt lgkmcnt(5)
	v_mfma_f32_32x32x16_f16 v[2:17], v[106:109], v[38:41], v[2:17]
	v_exp_f16_e64 v48, v46 clamp
	v_exp_f16_e64 v49, v47 clamp
	v_exp_f16_sdwa v48, v46 clamp dst_sel:WORD_1 dst_unused:UNUSED_PRESERVE src0_sel:WORD_1
	v_exp_f16_sdwa v49, v47 clamp dst_sel:WORD_1 dst_unused:UNUSED_PRESERVE src0_sel:WORD_1
	s_nop 0
	s_waitcnt lgkmcnt(4)
	v_mfma_f32_32x32x16_f16 v[2:17], v[82:85], v[50:53], v[2:17]
	v_pk_fma_f16 v38, v49, s20, v122 op_sel_hi:[1,0,0]
	s_nop 0
	v_pk_max_f16 v61, v47, v38
	v_pk_fma_f16 v38, v48, s20, v122 op_sel_hi:[1,0,0]
	s_nop 0
	v_pk_max_f16 v60, v46, v38
	s_waitcnt lgkmcnt(3)
	v_mfma_f32_32x32x16_f16 v[2:17], v[110:113], v[54:57], v[2:17]
	v_mfma_f32_16x16x32_f16 v[30:33], v[66:69], v[58:61], v[30:33]
	s_waitcnt lgkmcnt(2)
	v_mfma_f32_32x32x16_f16 v[2:17], v[94:97], v[42:45], v[2:17]
	s_waitcnt lgkmcnt(1)
	v_mfma_f32_32x32x16_f16 v[2:17], v[134:137], v[34:37], v[2:17]
	s_waitcnt lgkmcnt(0)
	v_mfma_f32_32x32x16_f16 v[2:17], v[130:133], v[62:65], v[2:17]
	s_nop 5
	ds_write2_b32 v211, v30, v31 offset1:1
	s_and_saveexec_b64 s[20:21], s[0:1]
	ds_write2_b32 v211, v32, v33 offset0:2 offset1:3
	s_or_b64 exec, exec, s[20:21]
	s_sub_i32 s20, 0x7a, s30
	s_mul_i32 s20, s20, 6
	s_ashr_i32 s21, s20, 31
	s_add_u32 s12, s12, s20
	s_addc_u32 s13, s13, s21
	s_and_b64 vcc, exec, s[8:9]
	s_waitcnt lgkmcnt(0)
	s_barrier
	s_cbranch_vccnz .LBB1_216
	s_cmp_lg_u32 s41, 0
	s_cbranch_scc0 .LBB1_212
	s_and_saveexec_b64 s[20:21], s[4:5]
	s_cbranch_execz .LBB1_211
	ds_read2_b32 v[18:19], v200 offset1:224
	v_add_u32_e32 v20, 0x700, v200
	ds_read2_b32 v[20:21], v20 offset1:224
	v_add_u32_e32 v22, 0xe00, v200
	ds_read2_b32 v[22:23], v22 offset1:224
	v_add_u32_e32 v24, 0x1500, v200
	ds_read2_b32 v[24:25], v24 offset1:224
	ds_read_b32 v26, v200 offset:448
	ds_read_b32 v27, v200 offset:1344
	ds_read_b32 v28, v200 offset:2240
	ds_read_b32 v29, v200 offset:3136
	ds_read_b32 v30, v200 offset:4032
	ds_read_b32 v31, v200 offset:4928
	ds_read_b32 v32, v200 offset:5824
	ds_read_b32 v33, v200 offset:6720
	s_waitcnt lgkmcnt(8)
	v_add_f32_e32 v18, 0, v18
	v_add_f32_e32 v18, v18, v19
	v_add_f32_e32 v18, v18, v20
	v_add_f32_e32 v18, v18, v21
	v_add_f32_e32 v18, v18, v22
	v_add_f32_e32 v18, v18, v23
	v_add_f32_e32 v18, v18, v24
	v_add_f32_e32 v18, v18, v25
	s_waitcnt lgkmcnt(0)
	v_add_f32_e32 v26, 0, v26
	v_add_f32_e32 v26, v26, v27
	v_add_f32_e32 v26, v26, v28
	v_add_f32_e32 v26, v26, v29
	v_add_f32_e32 v26, v26, v30
	v_add_f32_e32 v26, v26, v31
	v_add_f32_e32 v26, v26, v32
	v_add_f32_e32 v26, v26, v33
	v_mov_b32_e32 v19, 0x19280
	v_lshl_add_u32 v19, v177, 2, v19
	ds_write_b32 v19, v18
	ds_write_b32 v19, v26 offset:64

.LBB1_216:
	s_sub_i32 s20, 0x79, s30
	s_mul_i32 s20, s20, 6
	s_ashr_i32 s21, s20, 31
	s_add_u32 s12, s12, s20
	s_addc_u32 s13, s13, s21
	s_cmp_lg_u32 s41, 0
	s_cselect_b64 vcc, s[74:75], s[74:75]
	s_and_b64 vcc, exec, vcc
	s_cbranch_vccnz .LBB1_225
	s_cmp_lg_u32 s41, 0
	s_cbranch_scc0 .LBB1_221
	s_and_saveexec_b64 s[20:21], s[4:5]
	s_cbranch_execz .LBB1_220
	ds_read2_b32 v[18:19], v190 offset1:224
	v_add_u32_e32 v20, 0x700, v190
	ds_read2_b32 v[20:21], v20 offset1:224
	v_add_u32_e32 v22, 0xe00, v190
	ds_read2_b32 v[22:23], v22 offset1:224
	v_add_u32_e32 v24, 0x1500, v190
	ds_read2_b32 v[24:25], v24 offset1:224
	ds_read_b32 v26, v190 offset:448
	ds_read_b32 v27, v190 offset:1344
	ds_read_b32 v28, v190 offset:2240
	ds_read_b32 v29, v190 offset:3136
	ds_read_b32 v30, v190 offset:4032
	ds_read_b32 v31, v190 offset:4928
	ds_read_b32 v32, v190 offset:5824
	ds_read_b32 v33, v190 offset:6720
	s_waitcnt lgkmcnt(8)
	v_add_f32_e32 v18, 0, v18
	v_add_f32_e32 v18, v18, v19
	v_add_f32_e32 v18, v18, v20
	v_add_f32_e32 v18, v18, v21
	v_add_f32_e32 v18, v18, v22
	v_add_f32_e32 v18, v18, v23
	v_add_f32_e32 v18, v18, v24
	v_add_f32_e32 v18, v18, v25
	s_waitcnt lgkmcnt(0)
	v_add_f32_e32 v26, 0, v26
	v_add_f32_e32 v26, v26, v27
	v_add_f32_e32 v26, v26, v28
	v_add_f32_e32 v26, v26, v29
	v_add_f32_e32 v26, v26, v30
	v_add_f32_e32 v26, v26, v31
	v_add_f32_e32 v26, v26, v32
	v_add_f32_e32 v26, v26, v33
	v_mov_b32_e32 v19, 0x19300
	v_lshl_add_u32 v19, v177, 2, v19
	ds_write_b32 v19, v18
	ds_write_b32 v19, v26 offset:64

.LBB1_225:
	v_cvt_pk_f16_f32 v2, v2, v3
	v_cvt_pk_f16_f32 v3, v4, v5
	v_exp_f16_e64 v4, v2 clamp
	v_exp_f16_e64 v5, v3 clamp
	v_exp_f16_sdwa v4, v2 clamp dst_sel:WORD_1 dst_unused:UNUSED_PRESERVE src0_sel:WORD_1
	v_exp_f16_sdwa v5, v3 clamp dst_sel:WORD_1 dst_unused:UNUSED_PRESERVE src0_sel:WORD_1
	s_nop 0
	s_movk_i32 s20, 0x3dc5
	v_mov_b32_e32 v34, 0xbdc5
	v_pk_fma_f16 v5, v5, s20, v34 op_sel_hi:[1,0,0]
	v_pk_fma_f16 v4, v4, s20, v34 op_sel_hi:[1,0,0]
	v_pk_max_f16 v3, v3, v5
	v_pk_max_f16 v2, v2, v4
	v_cvt_pk_f16_f32 v4, v6, v7
	v_cvt_pk_f16_f32 v5, v8, v9
	v_exp_f16_e64 v6, v4 clamp
	v_exp_f16_e64 v7, v5 clamp
	v_exp_f16_sdwa v6, v4 clamp dst_sel:WORD_1 dst_unused:UNUSED_PRESERVE src0_sel:WORD_1
	v_exp_f16_sdwa v7, v5 clamp dst_sel:WORD_1 dst_unused:UNUSED_PRESERVE src0_sel:WORD_1
	s_nop 0
	s_nop 0
	v_pk_fma_f16 v7, v7, s20, v34 op_sel_hi:[1,0,0]
	v_pk_fma_f16 v6, v6, s20, v34 op_sel_hi:[1,0,0]
	v_pk_max_f16 v5, v5, v7
	v_pk_max_f16 v4, v4, v6
	s_nop 1
	v_mfma_f32_16x16x32_f16 v[30:33], v[70:73], v[2:5], 0
	v_cvt_pk_f16_f32 v6, v10, v11
	v_cvt_pk_f16_f32 v7, v12, v13
	v_exp_f16_e64 v2, v6 clamp
	v_exp_f16_e64 v3, v7 clamp
	v_exp_f16_sdwa v2, v6 clamp dst_sel:WORD_1 dst_unused:UNUSED_PRESERVE src0_sel:WORD_1
	v_exp_f16_sdwa v3, v7 clamp dst_sel:WORD_1 dst_unused:UNUSED_PRESERVE src0_sel:WORD_1
	s_nop 0
	s_nop 0
	v_pk_fma_f16 v3, v3, s20, v34 op_sel_hi:[1,0,0]
	v_pk_fma_f16 v2, v2, s20, v34 op_sel_hi:[1,0,0]
	v_pk_max_f16 v3, v7, v3
	v_pk_max_f16 v2, v6, v2
	v_cvt_pk_f16_f32 v4, v14, v15
	v_cvt_pk_f16_f32 v5, v16, v17
	v_exp_f16_e64 v6, v4 clamp
	v_exp_f16_e64 v7, v5 clamp
	v_exp_f16_sdwa v6, v4 clamp dst_sel:WORD_1 dst_unused:UNUSED_PRESERVE src0_sel:WORD_1
	v_exp_f16_sdwa v7, v5 clamp dst_sel:WORD_1 dst_unused:UNUSED_PRESERVE src0_sel:WORD_1
	s_nop 0
	s_nop 0
	v_pk_fma_f16 v7, v7, s20, v34 op_sel_hi:[1,0,0]
	v_pk_fma_f16 v6, v6, s20, v34 op_sel_hi:[1,0,0]
	v_pk_max_f16 v5, v5, v7
	v_pk_max_f16 v4, v4, v6
	s_nop 1
	v_mfma_f32_16x16x32_f16 v[30:33], v[66:69], v[2:5], v[30:33]
	v_mul_lo_u32 v2, v178, 28
	v_lshlrev_b32_e32 v1, 2, v1
	s_mov_b32 s20, 0x15c00
	v_add3_u32 v1, v2, v1, s20
	s_nop 7
	ds_write2_b32 v1, v30, v31 offset1:1
	s_and_saveexec_b64 s[20:21], s[0:1]
	ds_write2_b32 v1, v32, v33 offset0:2 offset1:3
	s_or_b64 exec, exec, s[20:21]
	s_and_b64 vcc, exec, s[8:9]
	s_waitcnt lgkmcnt(0)
	s_barrier
	s_cbranch_vccnz .LBB1_234
	s_cmp_lg_u32 s41, 0
	s_cbranch_scc0 .LBB1_237
	s_and_saveexec_b64 s[0:1], s[4:5]
	s_cbranch_execz .LBB1_233
	ds_read2_b32 v[2:3], v180 offset1:224
	v_add_u32_e32 v4, 0x700, v180
	ds_read2_b32 v[4:5], v4 offset1:224
	v_add_u32_e32 v6, 0xe00, v180
	ds_read2_b32 v[6:7], v6 offset1:224
	v_add_u32_e32 v8, 0x1500, v180
	ds_read2_b32 v[8:9], v8 offset1:224
	ds_read_b32 v10, v180 offset:448
	ds_read_b32 v11, v180 offset:1344
	ds_read_b32 v12, v180 offset:2240
	ds_read_b32 v13, v180 offset:3136
	ds_read_b32 v14, v180 offset:4032
	ds_read_b32 v15, v180 offset:4928
	ds_read_b32 v16, v180 offset:5824
	ds_read_b32 v17, v180 offset:6720
	s_waitcnt lgkmcnt(8)
	v_add_f32_e32 v1, 0, v2
	v_add_f32_e32 v1, v1, v3
	v_add_f32_e32 v1, v1, v4
	v_add_f32_e32 v1, v1, v5
	v_add_f32_e32 v1, v1, v6
	v_add_f32_e32 v1, v1, v7
	v_add_f32_e32 v1, v1, v8
	v_add_f32_e32 v1, v1, v9
	s_waitcnt lgkmcnt(0)
	v_add_f32_e32 v10, 0, v10
	v_add_f32_e32 v10, v10, v11
	v_add_f32_e32 v10, v10, v12
	v_add_f32_e32 v10, v10, v13
	v_add_f32_e32 v10, v10, v14
	v_add_f32_e32 v10, v10, v15
	v_add_f32_e32 v10, v10, v16
	v_add_f32_e32 v10, v10, v17
	v_mov_b32_e32 v2, 0x19380
	v_lshl_add_u32 v2, v177, 2, v2
	ds_write_b32 v2, v1
	ds_write_b32 v2, v10 offset:64
